# E1/E2: MFMA-result padding before the output stage trimmed from 16 to the required 8 wait states
# baseline (speedup 1.0000x reference)
.Le1_no6:
	s_lshr_b32 s99, s38, 4
	s_add_i32 m0, s99, 0x21200
	s_mov_b32 exec_hi, 0
	global_load_lds_dwordx4 v150, s[2:3]
	s_mov_b32 exec_hi, -1
	v_add_u32_e32 v150, s40, v150
	s_lshr_b32 s99, s38, 5
	s_add_i32 m0, s99, 0x23000
	s_mov_b64 exec, 0xffff
	global_load_lds_dwordx4 v149, s[22:23]
	s_mov_b64 exec, -1
	v_add_u32_e32 v149, 0x100, v149
	s_waitcnt vmcnt(15)
	ds_read_b128 v[90:93], v146 offset:2048
	ds_read_b128 v[94:97], v147 offset:2048
	s_waitcnt lgkmcnt(2)
	s_add_i32 m0, s38, 0x0
	v_mad_u32_u16 v142, v74, v249, v144
	global_load_lds_dwordx4 v142, s[10:11]
	s_add_i32 m0, s38, 0x400
	v_mad_u32_u16 v143, v78, v249, v145
	global_load_lds_dwordx4 v143, s[10:11]
	v_cvt_scalef32_pk_bf16_fp4 v98, v82, 1.0
	v_cvt_scalef32_pk_bf16_fp4 v99, v82, 1.0 op_sel:[1,0,0]
	v_cvt_scalef32_pk_bf16_fp4 v100, v82, 1.0 op_sel:[0,1,0]
	v_cvt_scalef32_pk_bf16_fp4 v101, v82, 1.0 op_sel:[1,1,0]
	v_cvt_scalef32_pk_bf16_fp4 v102, v83, 1.0
	v_cvt_scalef32_pk_bf16_fp4 v103, v83, 1.0 op_sel:[1,0,0]
	v_cvt_scalef32_pk_bf16_fp4 v104, v83, 1.0 op_sel:[0,1,0]
	v_cvt_scalef32_pk_bf16_fp4 v105, v83, 1.0 op_sel:[1,1,0]
	v_mfma_f32_16x16x32_bf16 v[106:109], v[2:5], v[98:101], 0
	v_cvt_scalef32_pk_bf16_fp4 v98, v84, 1.0
	v_cvt_scalef32_pk_bf16_fp4 v99, v84, 1.0 op_sel:[1,0,0]
	v_cvt_scalef32_pk_bf16_fp4 v100, v84, 1.0 op_sel:[0,1,0]
	v_cvt_scalef32_pk_bf16_fp4 v101, v84, 1.0 op_sel:[1,1,0]
	v_mfma_f32_16x16x32_bf16 v[106:109], v[6:9], v[102:105], v[106:109]
	v_cvt_scalef32_pk_bf16_fp4 v102, v85, 1.0
	v_cvt_scalef32_pk_bf16_fp4 v103, v85, 1.0 op_sel:[1,0,0]
	v_cvt_scalef32_pk_bf16_fp4 v104, v85, 1.0 op_sel:[0,1,0]
	v_cvt_scalef32_pk_bf16_fp4 v105, v85, 1.0 op_sel:[1,1,0]
	v_mfma_f32_16x16x32_bf16 v[106:109], v[10:13], v[98:101], v[106:109]
	v_cvt_scalef32_pk_bf16_fp4 v98, v86, 1.0
	v_cvt_scalef32_pk_bf16_fp4 v99, v86, 1.0 op_sel:[1,0,0]
	v_cvt_scalef32_pk_bf16_fp4 v100, v86, 1.0 op_sel:[0,1,0]
	v_cvt_scalef32_pk_bf16_fp4 v101, v86, 1.0 op_sel:[1,1,0]
	v_mfma_f32_16x16x32_bf16 v[106:109], v[14:17], v[102:105], v[106:109]
	v_cvt_scalef32_pk_bf16_fp4 v102, v87, 1.0
	v_cvt_scalef32_pk_bf16_fp4 v103, v87, 1.0 op_sel:[1,0,0]
	v_cvt_scalef32_pk_bf16_fp4 v104, v87, 1.0 op_sel:[0,1,0]
	v_cvt_scalef32_pk_bf16_fp4 v105, v87, 1.0 op_sel:[1,1,0]
	v_mfma_f32_16x16x32_bf16 v[106:109], v[18:21], v[98:101], v[106:109]
	v_cvt_scalef32_pk_bf16_fp4 v98, v88, 1.0
	v_cvt_scalef32_pk_bf16_fp4 v99, v88, 1.0 op_sel:[1,0,0]
	v_cvt_scalef32_pk_bf16_fp4 v100, v88, 1.0 op_sel:[0,1,0]
	v_cvt_scalef32_pk_bf16_fp4 v101, v88, 1.0 op_sel:[1,1,0]
	v_mfma_f32_16x16x32_bf16 v[106:109], v[22:25], v[102:105], v[106:109]
	v_cvt_scalef32_pk_bf16_fp4 v102, v89, 1.0
	v_cvt_scalef32_pk_bf16_fp4 v103, v89, 1.0 op_sel:[1,0,0]
	v_cvt_scalef32_pk_bf16_fp4 v104, v89, 1.0 op_sel:[0,1,0]
	v_cvt_scalef32_pk_bf16_fp4 v105, v89, 1.0 op_sel:[1,1,0]
	v_mfma_f32_16x16x32_bf16 v[106:109], v[26:29], v[98:101], v[106:109]
	v_mfma_f32_16x16x32_bf16 v[106:109], v[30:33], v[102:105], v[106:109]
	s_waitcnt vmcnt(15)
	ds_read_b128 v[82:85], v146 offset:4096
	ds_read_b128 v[86:89], v147 offset:4096
	s_waitcnt lgkmcnt(2)
	s_add_i32 m0, s38, 0x800
	v_mad_u32_u16 v142, v74, v249, v144 op_sel:[1,0,0,0]
	global_load_lds_dwordx4 v142, s[10:11]
	s_add_i32 m0, s38, 0xc00
	v_mad_u32_u16 v143, v78, v249, v145 op_sel:[1,0,0,0]
	global_load_lds_dwordx4 v143, s[10:11]
	v_cvt_scalef32_pk_bf16_fp4 v98, v90, 1.0
	v_cvt_scalef32_pk_bf16_fp4 v99, v90, 1.0 op_sel:[1,0,0]
	v_cvt_scalef32_pk_bf16_fp4 v100, v90, 1.0 op_sel:[0,1,0]
	v_cvt_scalef32_pk_bf16_fp4 v101, v90, 1.0 op_sel:[1,1,0]
	v_cvt_scalef32_pk_bf16_fp4 v102, v91, 1.0
	v_cvt_scalef32_pk_bf16_fp4 v103, v91, 1.0 op_sel:[1,0,0]
	v_cvt_scalef32_pk_bf16_fp4 v104, v91, 1.0 op_sel:[0,1,0]
	v_cvt_scalef32_pk_bf16_fp4 v105, v91, 1.0 op_sel:[1,1,0]
	v_mfma_f32_16x16x32_bf16 v[110:113], v[2:5], v[98:101], 0
	v_cvt_scalef32_pk_bf16_fp4 v98, v92, 1.0
	v_cvt_scalef32_pk_bf16_fp4 v99, v92, 1.0 op_sel:[1,0,0]
	v_cvt_scalef32_pk_bf16_fp4 v100, v92, 1.0 op_sel:[0,1,0]
	v_cvt_scalef32_pk_bf16_fp4 v101, v92, 1.0 op_sel:[1,1,0]
	v_mfma_f32_16x16x32_bf16 v[110:113], v[6:9], v[102:105], v[110:113]
	v_cvt_scalef32_pk_bf16_fp4 v102, v93, 1.0
	v_cvt_scalef32_pk_bf16_fp4 v103, v93, 1.0 op_sel:[1,0,0]
	v_cvt_scalef32_pk_bf16_fp4 v104, v93, 1.0 op_sel:[0,1,0]
	v_cvt_scalef32_pk_bf16_fp4 v105, v93, 1.0 op_sel:[1,1,0]
	v_mfma_f32_16x16x32_bf16 v[110:113], v[10:13], v[98:101], v[110:113]
	v_cvt_scalef32_pk_bf16_fp4 v98, v94, 1.0
	v_cvt_scalef32_pk_bf16_fp4 v99, v94, 1.0 op_sel:[1,0,0]
	v_cvt_scalef32_pk_bf16_fp4 v100, v94, 1.0 op_sel:[0,1,0]
	v_cvt_scalef32_pk_bf16_fp4 v101, v94, 1.0 op_sel:[1,1,0]
	v_mfma_f32_16x16x32_bf16 v[110:113], v[14:17], v[102:105], v[110:113]
	v_cvt_scalef32_pk_bf16_fp4 v102, v95, 1.0
	v_cvt_scalef32_pk_bf16_fp4 v103, v95, 1.0 op_sel:[1,0,0]
	v_cvt_scalef32_pk_bf16_fp4 v104, v95, 1.0 op_sel:[0,1,0]
	v_cvt_scalef32_pk_bf16_fp4 v105, v95, 1.0 op_sel:[1,1,0]
	v_mfma_f32_16x16x32_bf16 v[110:113], v[18:21], v[98:101], v[110:113]
	v_cvt_scalef32_pk_bf16_fp4 v98, v96, 1.0
	v_cvt_scalef32_pk_bf16_fp4 v99, v96, 1.0 op_sel:[1,0,0]
	v_cvt_scalef32_pk_bf16_fp4 v100, v96, 1.0 op_sel:[0,1,0]
	v_cvt_scalef32_pk_bf16_fp4 v101, v96, 1.0 op_sel:[1,1,0]
	v_mfma_f32_16x16x32_bf16 v[110:113], v[22:25], v[102:105], v[110:113]
	v_cvt_scalef32_pk_bf16_fp4 v102, v97, 1.0
	v_cvt_scalef32_pk_bf16_fp4 v103, v97, 1.0 op_sel:[1,0,0]
	v_cvt_scalef32_pk_bf16_fp4 v104, v97, 1.0 op_sel:[0,1,0]
	v_cvt_scalef32_pk_bf16_fp4 v105, v97, 1.0 op_sel:[1,1,0]
	v_mfma_f32_16x16x32_bf16 v[110:113], v[26:29], v[98:101], v[110:113]
	v_mfma_f32_16x16x32_bf16 v[110:113], v[30:33], v[102:105], v[110:113]
	s_waitcnt vmcnt(15)
	ds_read_b128 v[90:93], v146 offset:6144
	ds_read_b128 v[94:97], v147 offset:6144
	s_waitcnt lgkmcnt(2)
	s_add_i32 m0, s38, 0x1000
	v_mad_u32_u16 v142, v75, v249, v144
	global_load_lds_dwordx4 v142, s[10:11]
	s_add_i32 m0, s38, 0x1400
	v_mad_u32_u16 v143, v79, v249, v145
	global_load_lds_dwordx4 v143, s[10:11]
	v_cvt_scalef32_pk_bf16_fp4 v98, v82, 1.0
	v_cvt_scalef32_pk_bf16_fp4 v99, v82, 1.0 op_sel:[1,0,0]
	v_cvt_scalef32_pk_bf16_fp4 v100, v82, 1.0 op_sel:[0,1,0]
	v_cvt_scalef32_pk_bf16_fp4 v101, v82, 1.0 op_sel:[1,1,0]
	v_cvt_scalef32_pk_bf16_fp4 v102, v83, 1.0
	v_cvt_scalef32_pk_bf16_fp4 v103, v83, 1.0 op_sel:[1,0,0]
	v_cvt_scalef32_pk_bf16_fp4 v104, v83, 1.0 op_sel:[0,1,0]
	v_cvt_scalef32_pk_bf16_fp4 v105, v83, 1.0 op_sel:[1,1,0]
	v_mfma_f32_16x16x32_bf16 v[114:117], v[2:5], v[98:101], 0
	v_cvt_scalef32_pk_bf16_fp4 v98, v84, 1.0
	v_cvt_scalef32_pk_bf16_fp4 v99, v84, 1.0 op_sel:[1,0,0]
	v_cvt_scalef32_pk_bf16_fp4 v100, v84, 1.0 op_sel:[0,1,0]
	v_cvt_scalef32_pk_bf16_fp4 v101, v84, 1.0 op_sel:[1,1,0]
	v_mfma_f32_16x16x32_bf16 v[114:117], v[6:9], v[102:105], v[114:117]
	v_cvt_scalef32_pk_bf16_fp4 v102, v85, 1.0
	v_cvt_scalef32_pk_bf16_fp4 v103, v85, 1.0 op_sel:[1,0,0]
	v_cvt_scalef32_pk_bf16_fp4 v104, v85, 1.0 op_sel:[0,1,0]
	v_cvt_scalef32_pk_bf16_fp4 v105, v85, 1.0 op_sel:[1,1,0]
	v_mfma_f32_16x16x32_bf16 v[114:117], v[10:13], v[98:101], v[114:117]
	v_cvt_scalef32_pk_bf16_fp4 v98, v86, 1.0
	v_cvt_scalef32_pk_bf16_fp4 v99, v86, 1.0 op_sel:[1,0,0]
	v_cvt_scalef32_pk_bf16_fp4 v100, v86, 1.0 op_sel:[0,1,0]
	v_cvt_scalef32_pk_bf16_fp4 v101, v86, 1.0 op_sel:[1,1,0]
	v_mfma_f32_16x16x32_bf16 v[114:117], v[14:17], v[102:105], v[114:117]
	v_cvt_scalef32_pk_bf16_fp4 v102, v87, 1.0
	v_cvt_scalef32_pk_bf16_fp4 v103, v87, 1.0 op_sel:[1,0,0]
	v_cvt_scalef32_pk_bf16_fp4 v104, v87, 1.0 op_sel:[0,1,0]
	v_cvt_scalef32_pk_bf16_fp4 v105, v87, 1.0 op_sel:[1,1,0]
	v_mfma_f32_16x16x32_bf16 v[114:117], v[18:21], v[98:101], v[114:117]
	v_cvt_scalef32_pk_bf16_fp4 v98, v88, 1.0
	v_cvt_scalef32_pk_bf16_fp4 v99, v88, 1.0 op_sel:[1,0,0]
	v_cvt_scalef32_pk_bf16_fp4 v100, v88, 1.0 op_sel:[0,1,0]
	v_cvt_scalef32_pk_bf16_fp4 v101, v88, 1.0 op_sel:[1,1,0]
	v_mfma_f32_16x16x32_bf16 v[114:117], v[22:25], v[102:105], v[114:117]
	v_cvt_scalef32_pk_bf16_fp4 v102, v89, 1.0
	v_cvt_scalef32_pk_bf16_fp4 v103, v89, 1.0 op_sel:[1,0,0]
	v_cvt_scalef32_pk_bf16_fp4 v104, v89, 1.0 op_sel:[0,1,0]
	v_cvt_scalef32_pk_bf16_fp4 v105, v89, 1.0 op_sel:[1,1,0]
	v_mfma_f32_16x16x32_bf16 v[114:117], v[26:29], v[98:101], v[114:117]
	v_mfma_f32_16x16x32_bf16 v[114:117], v[30:33], v[102:105], v[114:117]
	s_waitcnt vmcnt(15)
	ds_read_b128 v[82:85], v146 offset:8192
	ds_read_b128 v[86:89], v147 offset:8192
	s_waitcnt lgkmcnt(2)
	s_add_i32 m0, s38, 0x1800
	v_mad_u32_u16 v142, v75, v249, v144 op_sel:[1,0,0,0]
	global_load_lds_dwordx4 v142, s[10:11]
	s_add_i32 m0, s38, 0x1c00
	v_mad_u32_u16 v143, v79, v249, v145 op_sel:[1,0,0,0]
	global_load_lds_dwordx4 v143, s[10:11]
	v_cvt_scalef32_pk_bf16_fp4 v98, v90, 1.0
	v_cvt_scalef32_pk_bf16_fp4 v99, v90, 1.0 op_sel:[1,0,0]
	v_cvt_scalef32_pk_bf16_fp4 v100, v90, 1.0 op_sel:[0,1,0]
	v_cvt_scalef32_pk_bf16_fp4 v101, v90, 1.0 op_sel:[1,1,0]
	v_cvt_scalef32_pk_bf16_fp4 v102, v91, 1.0
	v_cvt_scalef32_pk_bf16_fp4 v103, v91, 1.0 op_sel:[1,0,0]
	v_cvt_scalef32_pk_bf16_fp4 v104, v91, 1.0 op_sel:[0,1,0]
	v_cvt_scalef32_pk_bf16_fp4 v105, v91, 1.0 op_sel:[1,1,0]
	v_mfma_f32_16x16x32_bf16 v[118:121], v[2:5], v[98:101], 0
	v_cvt_scalef32_pk_bf16_fp4 v98, v92, 1.0
	v_cvt_scalef32_pk_bf16_fp4 v99, v92, 1.0 op_sel:[1,0,0]
	v_cvt_scalef32_pk_bf16_fp4 v100, v92, 1.0 op_sel:[0,1,0]
	v_cvt_scalef32_pk_bf16_fp4 v101, v92, 1.0 op_sel:[1,1,0]
	v_mfma_f32_16x16x32_bf16 v[118:121], v[6:9], v[102:105], v[118:121]
	v_cvt_scalef32_pk_bf16_fp4 v102, v93, 1.0
	v_cvt_scalef32_pk_bf16_fp4 v103, v93, 1.0 op_sel:[1,0,0]
	v_cvt_scalef32_pk_bf16_fp4 v104, v93, 1.0 op_sel:[0,1,0]
	v_cvt_scalef32_pk_bf16_fp4 v105, v93, 1.0 op_sel:[1,1,0]
	v_mfma_f32_16x16x32_bf16 v[118:121], v[10:13], v[98:101], v[118:121]
	v_cvt_scalef32_pk_bf16_fp4 v98, v94, 1.0
	v_cvt_scalef32_pk_bf16_fp4 v99, v94, 1.0 op_sel:[1,0,0]
	v_cvt_scalef32_pk_bf16_fp4 v100, v94, 1.0 op_sel:[0,1,0]
	v_cvt_scalef32_pk_bf16_fp4 v101, v94, 1.0 op_sel:[1,1,0]
	v_mfma_f32_16x16x32_bf16 v[118:121], v[14:17], v[102:105], v[118:121]
	v_cvt_scalef32_pk_bf16_fp4 v102, v95, 1.0
	v_cvt_scalef32_pk_bf16_fp4 v103, v95, 1.0 op_sel:[1,0,0]
	v_cvt_scalef32_pk_bf16_fp4 v104, v95, 1.0 op_sel:[0,1,0]
	v_cvt_scalef32_pk_bf16_fp4 v105, v95, 1.0 op_sel:[1,1,0]
	v_mfma_f32_16x16x32_bf16 v[118:121], v[18:21], v[98:101], v[118:121]
	v_cvt_scalef32_pk_bf16_fp4 v98, v96, 1.0
	v_cvt_scalef32_pk_bf16_fp4 v99, v96, 1.0 op_sel:[1,0,0]
	v_cvt_scalef32_pk_bf16_fp4 v100, v96, 1.0 op_sel:[0,1,0]
	v_cvt_scalef32_pk_bf16_fp4 v101, v96, 1.0 op_sel:[1,1,0]
	v_mfma_f32_16x16x32_bf16 v[118:121], v[22:25], v[102:105], v[118:121]
	v_cvt_scalef32_pk_bf16_fp4 v102, v97, 1.0
	v_cvt_scalef32_pk_bf16_fp4 v103, v97, 1.0 op_sel:[1,0,0]
	v_cvt_scalef32_pk_bf16_fp4 v104, v97, 1.0 op_sel:[0,1,0]
	v_cvt_scalef32_pk_bf16_fp4 v105, v97, 1.0 op_sel:[1,1,0]
	v_mfma_f32_16x16x32_bf16 v[118:121], v[26:29], v[98:101], v[118:121]
	v_cvt_pk_bf16_f32 v138, v106, v110
	v_mfma_f32_16x16x32_bf16 v[118:121], v[30:33], v[102:105], v[118:121]
	s_waitcnt vmcnt(15)
	ds_read_b128 v[90:93], v146 offset:10240
	ds_read_b128 v[94:97], v147 offset:10240
	s_waitcnt lgkmcnt(2)
	s_add_i32 m0, s38, 0x2000
	v_mad_u32_u16 v142, v76, v249, v144
	global_load_lds_dwordx4 v142, s[10:11]
	s_add_i32 m0, s38, 0x2400
	v_mad_u32_u16 v143, v80, v249, v145
	global_load_lds_dwordx4 v143, s[10:11]
	v_cvt_scalef32_pk_bf16_fp4 v98, v82, 1.0
	v_cvt_scalef32_pk_bf16_fp4 v99, v82, 1.0 op_sel:[1,0,0]
	v_cvt_scalef32_pk_bf16_fp4 v100, v82, 1.0 op_sel:[0,1,0]
	v_cvt_scalef32_pk_bf16_fp4 v101, v82, 1.0 op_sel:[1,1,0]
	v_cvt_scalef32_pk_bf16_fp4 v102, v83, 1.0
	v_cvt_scalef32_pk_bf16_fp4 v103, v83, 1.0 op_sel:[1,0,0]
	v_cvt_scalef32_pk_bf16_fp4 v104, v83, 1.0 op_sel:[0,1,0]
	v_cvt_scalef32_pk_bf16_fp4 v105, v83, 1.0 op_sel:[1,1,0]
	v_mfma_f32_16x16x32_bf16 v[122:125], v[2:5], v[98:101], 0
	v_cvt_scalef32_pk_bf16_fp4 v98, v84, 1.0
	v_cvt_scalef32_pk_bf16_fp4 v99, v84, 1.0 op_sel:[1,0,0]
	v_cvt_scalef32_pk_bf16_fp4 v100, v84, 1.0 op_sel:[0,1,0]
	v_cvt_scalef32_pk_bf16_fp4 v101, v84, 1.0 op_sel:[1,1,0]
	v_mfma_f32_16x16x32_bf16 v[122:125], v[6:9], v[102:105], v[122:125]
	v_cvt_scalef32_pk_bf16_fp4 v102, v85, 1.0
	v_cvt_scalef32_pk_bf16_fp4 v103, v85, 1.0 op_sel:[1,0,0]
	v_cvt_scalef32_pk_bf16_fp4 v104, v85, 1.0 op_sel:[0,1,0]
	v_cvt_scalef32_pk_bf16_fp4 v105, v85, 1.0 op_sel:[1,1,0]
	v_mfma_f32_16x16x32_bf16 v[122:125], v[10:13], v[98:101], v[122:125]
	v_cvt_scalef32_pk_bf16_fp4 v98, v86, 1.0
	v_cvt_scalef32_pk_bf16_fp4 v99, v86, 1.0 op_sel:[1,0,0]
	v_cvt_scalef32_pk_bf16_fp4 v100, v86, 1.0 op_sel:[0,1,0]
	v_cvt_scalef32_pk_bf16_fp4 v101, v86, 1.0 op_sel:[1,1,0]
	v_mfma_f32_16x16x32_bf16 v[122:125], v[14:17], v[102:105], v[122:125]
	v_cvt_scalef32_pk_bf16_fp4 v102, v87, 1.0
	v_cvt_scalef32_pk_bf16_fp4 v103, v87, 1.0 op_sel:[1,0,0]
	v_cvt_scalef32_pk_bf16_fp4 v104, v87, 1.0 op_sel:[0,1,0]
	v_cvt_scalef32_pk_bf16_fp4 v105, v87, 1.0 op_sel:[1,1,0]
	v_mfma_f32_16x16x32_bf16 v[122:125], v[18:21], v[98:101], v[122:125]
	v_cvt_scalef32_pk_bf16_fp4 v98, v88, 1.0
	v_cvt_scalef32_pk_bf16_fp4 v99, v88, 1.0 op_sel:[1,0,0]
	v_cvt_scalef32_pk_bf16_fp4 v100, v88, 1.0 op_sel:[0,1,0]
	v_cvt_scalef32_pk_bf16_fp4 v101, v88, 1.0 op_sel:[1,1,0]
	v_mfma_f32_16x16x32_bf16 v[122:125], v[22:25], v[102:105], v[122:125]
	v_cvt_scalef32_pk_bf16_fp4 v102, v89, 1.0
	v_cvt_scalef32_pk_bf16_fp4 v103, v89, 1.0 op_sel:[1,0,0]
	v_cvt_scalef32_pk_bf16_fp4 v104, v89, 1.0 op_sel:[0,1,0]
	v_cvt_scalef32_pk_bf16_fp4 v105, v89, 1.0 op_sel:[1,1,0]
	v_mfma_f32_16x16x32_bf16 v[122:125], v[26:29], v[98:101], v[122:125]
	v_mfma_f32_16x16x32_bf16 v[122:125], v[30:33], v[102:105], v[122:125]
	s_waitcnt vmcnt(15)
	ds_read_b128 v[82:85], v146 offset:12288
	ds_read_b128 v[86:89], v147 offset:12288
	s_waitcnt lgkmcnt(2)
	s_add_i32 m0, s38, 0x2800
	v_mad_u32_u16 v142, v76, v249, v144 op_sel:[1,0,0,0]
	global_load_lds_dwordx4 v142, s[10:11]
	s_add_i32 m0, s38, 0x2c00
	v_mad_u32_u16 v143, v80, v249, v145 op_sel:[1,0,0,0]
	global_load_lds_dwordx4 v143, s[10:11]
	v_cvt_scalef32_pk_bf16_fp4 v98, v90, 1.0
	v_cvt_scalef32_pk_bf16_fp4 v99, v90, 1.0 op_sel:[1,0,0]
	v_cvt_scalef32_pk_bf16_fp4 v100, v90, 1.0 op_sel:[0,1,0]
	v_cvt_scalef32_pk_bf16_fp4 v101, v90, 1.0 op_sel:[1,1,0]
	v_cvt_scalef32_pk_bf16_fp4 v102, v91, 1.0
	v_cvt_scalef32_pk_bf16_fp4 v103, v91, 1.0 op_sel:[1,0,0]
	v_cvt_scalef32_pk_bf16_fp4 v104, v91, 1.0 op_sel:[0,1,0]
	v_cvt_scalef32_pk_bf16_fp4 v105, v91, 1.0 op_sel:[1,1,0]
	v_mfma_f32_16x16x32_bf16 v[126:129], v[2:5], v[98:101], 0
	v_cvt_scalef32_pk_bf16_fp4 v98, v92, 1.0
	v_cvt_scalef32_pk_bf16_fp4 v99, v92, 1.0 op_sel:[1,0,0]
	v_cvt_scalef32_pk_bf16_fp4 v100, v92, 1.0 op_sel:[0,1,0]
	v_cvt_scalef32_pk_bf16_fp4 v101, v92, 1.0 op_sel:[1,1,0]
	v_mfma_f32_16x16x32_bf16 v[126:129], v[6:9], v[102:105], v[126:129]
	v_cvt_scalef32_pk_bf16_fp4 v102, v93, 1.0
	v_cvt_scalef32_pk_bf16_fp4 v103, v93, 1.0 op_sel:[1,0,0]
	v_cvt_scalef32_pk_bf16_fp4 v104, v93, 1.0 op_sel:[0,1,0]
	v_cvt_scalef32_pk_bf16_fp4 v105, v93, 1.0 op_sel:[1,1,0]
	v_mfma_f32_16x16x32_bf16 v[126:129], v[10:13], v[98:101], v[126:129]
	v_cvt_scalef32_pk_bf16_fp4 v98, v94, 1.0
	v_cvt_scalef32_pk_bf16_fp4 v99, v94, 1.0 op_sel:[1,0,0]
	v_cvt_scalef32_pk_bf16_fp4 v100, v94, 1.0 op_sel:[0,1,0]
	v_cvt_scalef32_pk_bf16_fp4 v101, v94, 1.0 op_sel:[1,1,0]
	v_mfma_f32_16x16x32_bf16 v[126:129], v[14:17], v[102:105], v[126:129]
	v_cvt_scalef32_pk_bf16_fp4 v102, v95, 1.0
	v_cvt_scalef32_pk_bf16_fp4 v103, v95, 1.0 op_sel:[1,0,0]
	v_cvt_scalef32_pk_bf16_fp4 v104, v95, 1.0 op_sel:[0,1,0]
	v_cvt_scalef32_pk_bf16_fp4 v105, v95, 1.0 op_sel:[1,1,0]
	v_mfma_f32_16x16x32_bf16 v[126:129], v[18:21], v[98:101], v[126:129]
	v_cvt_scalef32_pk_bf16_fp4 v98, v96, 1.0
	v_cvt_scalef32_pk_bf16_fp4 v99, v96, 1.0 op_sel:[1,0,0]
	v_cvt_scalef32_pk_bf16_fp4 v100, v96, 1.0 op_sel:[0,1,0]
	v_cvt_scalef32_pk_bf16_fp4 v101, v96, 1.0 op_sel:[1,1,0]
	v_mfma_f32_16x16x32_bf16 v[126:129], v[22:25], v[102:105], v[126:129]
	v_cvt_scalef32_pk_bf16_fp4 v102, v97, 1.0
	v_cvt_scalef32_pk_bf16_fp4 v103, v97, 1.0 op_sel:[1,0,0]
	v_cvt_scalef32_pk_bf16_fp4 v104, v97, 1.0 op_sel:[0,1,0]
	v_cvt_scalef32_pk_bf16_fp4 v105, v97, 1.0 op_sel:[1,1,0]
	v_mfma_f32_16x16x32_bf16 v[126:129], v[26:29], v[98:101], v[126:129]
	v_cvt_pk_bf16_f32 v139, v114, v118
	v_mfma_f32_16x16x32_bf16 v[126:129], v[30:33], v[102:105], v[126:129]
	s_waitcnt vmcnt(15)
	ds_read_b128 v[90:93], v146 offset:14336
	ds_read_b128 v[94:97], v147 offset:14336
	s_waitcnt lgkmcnt(2)
	s_add_i32 m0, s38, 0x3000
	v_mad_u32_u16 v142, v77, v249, v144
	global_load_lds_dwordx4 v142, s[10:11]
	s_add_i32 m0, s38, 0x3400
	v_mad_u32_u16 v143, v81, v249, v145
	global_load_lds_dwordx4 v143, s[10:11]
	v_cvt_scalef32_pk_bf16_fp4 v98, v82, 1.0
	v_cvt_scalef32_pk_bf16_fp4 v99, v82, 1.0 op_sel:[1,0,0]
	v_cvt_scalef32_pk_bf16_fp4 v100, v82, 1.0 op_sel:[0,1,0]
	v_cvt_scalef32_pk_bf16_fp4 v101, v82, 1.0 op_sel:[1,1,0]
	v_cvt_scalef32_pk_bf16_fp4 v102, v83, 1.0
	v_cvt_scalef32_pk_bf16_fp4 v103, v83, 1.0 op_sel:[1,0,0]
	v_cvt_scalef32_pk_bf16_fp4 v104, v83, 1.0 op_sel:[0,1,0]
	v_cvt_scalef32_pk_bf16_fp4 v105, v83, 1.0 op_sel:[1,1,0]
	v_mfma_f32_16x16x32_bf16 v[130:133], v[2:5], v[98:101], 0
	v_cvt_scalef32_pk_bf16_fp4 v98, v84, 1.0
	v_cvt_scalef32_pk_bf16_fp4 v99, v84, 1.0 op_sel:[1,0,0]
	v_cvt_scalef32_pk_bf16_fp4 v100, v84, 1.0 op_sel:[0,1,0]
	v_cvt_scalef32_pk_bf16_fp4 v101, v84, 1.0 op_sel:[1,1,0]
	v_mfma_f32_16x16x32_bf16 v[130:133], v[6:9], v[102:105], v[130:133]
	v_cvt_scalef32_pk_bf16_fp4 v102, v85, 1.0
	v_cvt_scalef32_pk_bf16_fp4 v103, v85, 1.0 op_sel:[1,0,0]
	v_cvt_scalef32_pk_bf16_fp4 v104, v85, 1.0 op_sel:[0,1,0]
	v_cvt_scalef32_pk_bf16_fp4 v105, v85, 1.0 op_sel:[1,1,0]
	v_mfma_f32_16x16x32_bf16 v[130:133], v[10:13], v[98:101], v[130:133]
	v_cvt_scalef32_pk_bf16_fp4 v98, v86, 1.0
	v_cvt_scalef32_pk_bf16_fp4 v99, v86, 1.0 op_sel:[1,0,0]
	v_cvt_scalef32_pk_bf16_fp4 v100, v86, 1.0 op_sel:[0,1,0]
	v_cvt_scalef32_pk_bf16_fp4 v101, v86, 1.0 op_sel:[1,1,0]
	v_mfma_f32_16x16x32_bf16 v[130:133], v[14:17], v[102:105], v[130:133]
	v_cvt_scalef32_pk_bf16_fp4 v102, v87, 1.0
	v_cvt_scalef32_pk_bf16_fp4 v103, v87, 1.0 op_sel:[1,0,0]
	v_cvt_scalef32_pk_bf16_fp4 v104, v87, 1.0 op_sel:[0,1,0]
	v_cvt_scalef32_pk_bf16_fp4 v105, v87, 1.0 op_sel:[1,1,0]
	v_mfma_f32_16x16x32_bf16 v[130:133], v[18:21], v[98:101], v[130:133]
	v_cvt_scalef32_pk_bf16_fp4 v98, v88, 1.0
	v_cvt_scalef32_pk_bf16_fp4 v99, v88, 1.0 op_sel:[1,0,0]
	v_cvt_scalef32_pk_bf16_fp4 v100, v88, 1.0 op_sel:[0,1,0]
	v_cvt_scalef32_pk_bf16_fp4 v101, v88, 1.0 op_sel:[1,1,0]
	v_mfma_f32_16x16x32_bf16 v[130:133], v[22:25], v[102:105], v[130:133]
	v_cvt_scalef32_pk_bf16_fp4 v102, v89, 1.0
	v_cvt_scalef32_pk_bf16_fp4 v103, v89, 1.0 op_sel:[1,0,0]
	v_cvt_scalef32_pk_bf16_fp4 v104, v89, 1.0 op_sel:[0,1,0]
	v_cvt_scalef32_pk_bf16_fp4 v105, v89, 1.0 op_sel:[1,1,0]
	v_mfma_f32_16x16x32_bf16 v[130:133], v[26:29], v[98:101], v[130:133]
	v_mfma_f32_16x16x32_bf16 v[130:133], v[30:33], v[102:105], v[130:133]
	s_waitcnt vmcnt(12)
	ds_read_b128 v[82:85], v146
	ds_read_b128 v[86:89], v147
	s_waitcnt lgkmcnt(2)
	s_add_i32 m0, s38, 0x3800
	v_mad_u32_u16 v142, v77, v249, v144 op_sel:[1,0,0,0]
	global_load_lds_dwordx4 v142, s[10:11]
	s_add_i32 m0, s38, 0x3c00
	v_mad_u32_u16 v143, v81, v249, v145 op_sel:[1,0,0,0]
	global_load_lds_dwordx4 v143, s[10:11]
	ds_read_b128 v[34:37], v148 offset:512
	ds_read_b128 v[38:41], v148 offset:528
	ds_read_b128 v[42:45], v148 offset:544
	ds_read_b128 v[46:49], v148 offset:560
	ds_read_b128 v[50:53], v148 offset:768
	ds_read_b128 v[54:57], v148 offset:784
	ds_read_b128 v[58:61], v148 offset:800
	ds_read_b128 v[62:65], v148 offset:816
	ds_read_b128 v[66:69], v152
	ds_read_b128 v[70:73], v152 offset:16
	v_cvt_scalef32_pk_bf16_fp4 v98, v90, 1.0
	v_cvt_scalef32_pk_bf16_fp4 v99, v90, 1.0 op_sel:[1,0,0]
	v_cvt_scalef32_pk_bf16_fp4 v100, v90, 1.0 op_sel:[0,1,0]
	v_cvt_scalef32_pk_bf16_fp4 v101, v90, 1.0 op_sel:[1,1,0]
	v_cvt_scalef32_pk_bf16_fp4 v102, v91, 1.0
	v_cvt_scalef32_pk_bf16_fp4 v103, v91, 1.0 op_sel:[1,0,0]
	v_cvt_scalef32_pk_bf16_fp4 v104, v91, 1.0 op_sel:[0,1,0]
	v_cvt_scalef32_pk_bf16_fp4 v105, v91, 1.0 op_sel:[1,1,0]
	v_mfma_f32_16x16x32_bf16 v[134:137], v[2:5], v[98:101], 0
	v_cvt_scalef32_pk_bf16_fp4 v98, v92, 1.0
	v_cvt_scalef32_pk_bf16_fp4 v99, v92, 1.0 op_sel:[1,0,0]
	v_cvt_scalef32_pk_bf16_fp4 v100, v92, 1.0 op_sel:[0,1,0]
	v_cvt_scalef32_pk_bf16_fp4 v101, v92, 1.0 op_sel:[1,1,0]
	v_mfma_f32_16x16x32_bf16 v[134:137], v[6:9], v[102:105], v[134:137]
	v_cvt_scalef32_pk_bf16_fp4 v102, v93, 1.0
	v_cvt_scalef32_pk_bf16_fp4 v103, v93, 1.0 op_sel:[1,0,0]
	v_cvt_scalef32_pk_bf16_fp4 v104, v93, 1.0 op_sel:[0,1,0]
	v_cvt_scalef32_pk_bf16_fp4 v105, v93, 1.0 op_sel:[1,1,0]
	v_mfma_f32_16x16x32_bf16 v[134:137], v[10:13], v[98:101], v[134:137]
	v_cvt_scalef32_pk_bf16_fp4 v98, v94, 1.0
	v_cvt_scalef32_pk_bf16_fp4 v99, v94, 1.0 op_sel:[1,0,0]
	v_cvt_scalef32_pk_bf16_fp4 v100, v94, 1.0 op_sel:[0,1,0]
	v_cvt_scalef32_pk_bf16_fp4 v101, v94, 1.0 op_sel:[1,1,0]
	v_mfma_f32_16x16x32_bf16 v[134:137], v[14:17], v[102:105], v[134:137]
	v_cvt_scalef32_pk_bf16_fp4 v102, v95, 1.0
	v_cvt_scalef32_pk_bf16_fp4 v103, v95, 1.0 op_sel:[1,0,0]
	v_cvt_scalef32_pk_bf16_fp4 v104, v95, 1.0 op_sel:[0,1,0]
	v_cvt_scalef32_pk_bf16_fp4 v105, v95, 1.0 op_sel:[1,1,0]
	v_mfma_f32_16x16x32_bf16 v[134:137], v[18:21], v[98:101], v[134:137]
	v_cvt_scalef32_pk_bf16_fp4 v98, v96, 1.0
	v_cvt_scalef32_pk_bf16_fp4 v99, v96, 1.0 op_sel:[1,0,0]
	v_cvt_scalef32_pk_bf16_fp4 v100, v96, 1.0 op_sel:[0,1,0]
	v_cvt_scalef32_pk_bf16_fp4 v101, v96, 1.0 op_sel:[1,1,0]
	v_mfma_f32_16x16x32_bf16 v[134:137], v[22:25], v[102:105], v[134:137]
	v_cvt_scalef32_pk_bf16_fp4 v102, v97, 1.0
	v_cvt_scalef32_pk_bf16_fp4 v103, v97, 1.0 op_sel:[1,0,0]
	v_cvt_scalef32_pk_bf16_fp4 v104, v97, 1.0 op_sel:[0,1,0]
	v_cvt_scalef32_pk_bf16_fp4 v105, v97, 1.0 op_sel:[1,1,0]
	v_mfma_f32_16x16x32_bf16 v[134:137], v[26:29], v[98:101], v[134:137]
	v_cvt_pk_bf16_f32 v140, v122, v126
	v_mfma_f32_16x16x32_bf16 v[134:137], v[30:33], v[102:105], v[134:137]
	s_nop 7
	v_cvt_pk_bf16_f32 v141, v130, v134
	s_mov_b64 exec, 0xffff
	global_store_dwordx4 v151, v[138:141], s[4:5]
	s_mov_b64 exec, -1
	v_add_u32_e32 v151, 0x100, v151
	s_lshr_b32 s99, s38, 4
	s_add_i32 m0, s99, 0x21000
	s_mov_b32 exec_hi, 0
	global_load_lds_dwordx4 v150, s[2:3]
	s_mov_b32 exec_hi, -1
	v_add_u32_e32 v150, 0x1000, v150
	s_lshr_b32 s99, s38, 5
	s_add_i32 m0, s99, 0x23100
	s_mov_b64 exec, 0xffff
	global_load_lds_dwordx4 v149, s[22:23]
	s_mov_b64 exec, -1
	v_add_u32_e32 v149, s41, v149
	s_waitcnt vmcnt(15)
	ds_read_b128 v[90:93], v146 offset:2048
	ds_read_b128 v[94:97], v147 offset:2048
	s_waitcnt lgkmcnt(2)
	s_add_i32 m0, s38, 0x0
	v_mad_u32_u16 v142, v66, v249, v144
	global_load_lds_dwordx4 v142, s[10:11]
	s_add_i32 m0, s38, 0x400
	v_mad_u32_u16 v143, v70, v249, v145
	global_load_lds_dwordx4 v143, s[10:11]
	v_cvt_scalef32_pk_bf16_fp4 v98, v82, 1.0
	v_cvt_scalef32_pk_bf16_fp4 v99, v82, 1.0 op_sel:[1,0,0]
	v_cvt_scalef32_pk_bf16_fp4 v100, v82, 1.0 op_sel:[0,1,0]
	v_cvt_scalef32_pk_bf16_fp4 v101, v82, 1.0 op_sel:[1,1,0]
	v_cvt_scalef32_pk_bf16_fp4 v102, v83, 1.0
	v_cvt_scalef32_pk_bf16_fp4 v103, v83, 1.0 op_sel:[1,0,0]
	v_cvt_scalef32_pk_bf16_fp4 v104, v83, 1.0 op_sel:[0,1,0]
	v_cvt_scalef32_pk_bf16_fp4 v105, v83, 1.0 op_sel:[1,1,0]
	v_mfma_f32_16x16x32_bf16 v[106:109], v[34:37], v[98:101], 0
	v_cvt_scalef32_pk_bf16_fp4 v98, v84, 1.0
	v_cvt_scalef32_pk_bf16_fp4 v99, v84, 1.0 op_sel:[1,0,0]
	v_cvt_scalef32_pk_bf16_fp4 v100, v84, 1.0 op_sel:[0,1,0]
	v_cvt_scalef32_pk_bf16_fp4 v101, v84, 1.0 op_sel:[1,1,0]
	v_mfma_f32_16x16x32_bf16 v[106:109], v[38:41], v[102:105], v[106:109]
	v_cvt_scalef32_pk_bf16_fp4 v102, v85, 1.0
	v_cvt_scalef32_pk_bf16_fp4 v103, v85, 1.0 op_sel:[1,0,0]
	v_cvt_scalef32_pk_bf16_fp4 v104, v85, 1.0 op_sel:[0,1,0]
	v_cvt_scalef32_pk_bf16_fp4 v105, v85, 1.0 op_sel:[1,1,0]
	v_mfma_f32_16x16x32_bf16 v[106:109], v[42:45], v[98:101], v[106:109]
	v_cvt_scalef32_pk_bf16_fp4 v98, v86, 1.0
	v_cvt_scalef32_pk_bf16_fp4 v99, v86, 1.0 op_sel:[1,0,0]
	v_cvt_scalef32_pk_bf16_fp4 v100, v86, 1.0 op_sel:[0,1,0]
	v_cvt_scalef32_pk_bf16_fp4 v101, v86, 1.0 op_sel:[1,1,0]
	v_mfma_f32_16x16x32_bf16 v[106:109], v[46:49], v[102:105], v[106:109]
	v_cvt_scalef32_pk_bf16_fp4 v102, v87, 1.0
	v_cvt_scalef32_pk_bf16_fp4 v103, v87, 1.0 op_sel:[1,0,0]
	v_cvt_scalef32_pk_bf16_fp4 v104, v87, 1.0 op_sel:[0,1,0]
	v_cvt_scalef32_pk_bf16_fp4 v105, v87, 1.0 op_sel:[1,1,0]
	v_mfma_f32_16x16x32_bf16 v[106:109], v[50:53], v[98:101], v[106:109]
	v_cvt_scalef32_pk_bf16_fp4 v98, v88, 1.0
	v_cvt_scalef32_pk_bf16_fp4 v99, v88, 1.0 op_sel:[1,0,0]
	v_cvt_scalef32_pk_bf16_fp4 v100, v88, 1.0 op_sel:[0,1,0]
	v_cvt_scalef32_pk_bf16_fp4 v101, v88, 1.0 op_sel:[1,1,0]
	v_mfma_f32_16x16x32_bf16 v[106:109], v[54:57], v[102:105], v[106:109]
	v_cvt_scalef32_pk_bf16_fp4 v102, v89, 1.0
	v_cvt_scalef32_pk_bf16_fp4 v103, v89, 1.0 op_sel:[1,0,0]
	v_cvt_scalef32_pk_bf16_fp4 v104, v89, 1.0 op_sel:[0,1,0]
	v_cvt_scalef32_pk_bf16_fp4 v105, v89, 1.0 op_sel:[1,1,0]
	v_mfma_f32_16x16x32_bf16 v[106:109], v[58:61], v[98:101], v[106:109]
	v_mfma_f32_16x16x32_bf16 v[106:109], v[62:65], v[102:105], v[106:109]
	s_waitcnt vmcnt(15)
	ds_read_b128 v[82:85], v146 offset:4096
	ds_read_b128 v[86:89], v147 offset:4096
	s_waitcnt lgkmcnt(2)
	s_add_i32 m0, s38, 0x800
	v_mad_u32_u16 v142, v66, v249, v144 op_sel:[1,0,0,0]
	global_load_lds_dwordx4 v142, s[10:11]
	s_add_i32 m0, s38, 0xc00
	v_mad_u32_u16 v143, v70, v249, v145 op_sel:[1,0,0,0]
	global_load_lds_dwordx4 v143, s[10:11]
	v_cvt_scalef32_pk_bf16_fp4 v98, v90, 1.0
	v_cvt_scalef32_pk_bf16_fp4 v99, v90, 1.0 op_sel:[1,0,0]
	v_cvt_scalef32_pk_bf16_fp4 v100, v90, 1.0 op_sel:[0,1,0]
	v_cvt_scalef32_pk_bf16_fp4 v101, v90, 1.0 op_sel:[1,1,0]
	v_cvt_scalef32_pk_bf16_fp4 v102, v91, 1.0
	v_cvt_scalef32_pk_bf16_fp4 v103, v91, 1.0 op_sel:[1,0,0]
	v_cvt_scalef32_pk_bf16_fp4 v104, v91, 1.0 op_sel:[0,1,0]
	v_cvt_scalef32_pk_bf16_fp4 v105, v91, 1.0 op_sel:[1,1,0]
	v_mfma_f32_16x16x32_bf16 v[110:113], v[34:37], v[98:101], 0
	v_cvt_scalef32_pk_bf16_fp4 v98, v92, 1.0
	v_cvt_scalef32_pk_bf16_fp4 v99, v92, 1.0 op_sel:[1,0,0]
	v_cvt_scalef32_pk_bf16_fp4 v100, v92, 1.0 op_sel:[0,1,0]
	v_cvt_scalef32_pk_bf16_fp4 v101, v92, 1.0 op_sel:[1,1,0]
	v_mfma_f32_16x16x32_bf16 v[110:113], v[38:41], v[102:105], v[110:113]
	v_cvt_scalef32_pk_bf16_fp4 v102, v93, 1.0
	v_cvt_scalef32_pk_bf16_fp4 v103, v93, 1.0 op_sel:[1,0,0]
	v_cvt_scalef32_pk_bf16_fp4 v104, v93, 1.0 op_sel:[0,1,0]
	v_cvt_scalef32_pk_bf16_fp4 v105, v93, 1.0 op_sel:[1,1,0]
	v_mfma_f32_16x16x32_bf16 v[110:113], v[42:45], v[98:101], v[110:113]
	v_cvt_scalef32_pk_bf16_fp4 v98, v94, 1.0
	v_cvt_scalef32_pk_bf16_fp4 v99, v94, 1.0 op_sel:[1,0,0]
	v_cvt_scalef32_pk_bf16_fp4 v100, v94, 1.0 op_sel:[0,1,0]
	v_cvt_scalef32_pk_bf16_fp4 v101, v94, 1.0 op_sel:[1,1,0]
	v_mfma_f32_16x16x32_bf16 v[110:113], v[46:49], v[102:105], v[110:113]
	v_cvt_scalef32_pk_bf16_fp4 v102, v95, 1.0
	v_cvt_scalef32_pk_bf16_fp4 v103, v95, 1.0 op_sel:[1,0,0]
	v_cvt_scalef32_pk_bf16_fp4 v104, v95, 1.0 op_sel:[0,1,0]
	v_cvt_scalef32_pk_bf16_fp4 v105, v95, 1.0 op_sel:[1,1,0]
	v_mfma_f32_16x16x32_bf16 v[110:113], v[50:53], v[98:101], v[110:113]
	v_cvt_scalef32_pk_bf16_fp4 v98, v96, 1.0
	v_cvt_scalef32_pk_bf16_fp4 v99, v96, 1.0 op_sel:[1,0,0]
	v_cvt_scalef32_pk_bf16_fp4 v100, v96, 1.0 op_sel:[0,1,0]
	v_cvt_scalef32_pk_bf16_fp4 v101, v96, 1.0 op_sel:[1,1,0]
	v_mfma_f32_16x16x32_bf16 v[110:113], v[54:57], v[102:105], v[110:113]
	v_cvt_scalef32_pk_bf16_fp4 v102, v97, 1.0
	v_cvt_scalef32_pk_bf16_fp4 v103, v97, 1.0 op_sel:[1,0,0]
	v_cvt_scalef32_pk_bf16_fp4 v104, v97, 1.0 op_sel:[0,1,0]
	v_cvt_scalef32_pk_bf16_fp4 v105, v97, 1.0 op_sel:[1,1,0]
	v_mfma_f32_16x16x32_bf16 v[110:113], v[58:61], v[98:101], v[110:113]
	v_mfma_f32_16x16x32_bf16 v[110:113], v[62:65], v[102:105], v[110:113]
	s_waitcnt vmcnt(15)
	ds_read_b128 v[90:93], v146 offset:6144
	ds_read_b128 v[94:97], v147 offset:6144
	s_waitcnt lgkmcnt(2)
	s_add_i32 m0, s38, 0x1000
	v_mad_u32_u16 v142, v67, v249, v144
	global_load_lds_dwordx4 v142, s[10:11]
	s_add_i32 m0, s38, 0x1400
	v_mad_u32_u16 v143, v71, v249, v145
	global_load_lds_dwordx4 v143, s[10:11]
	v_cvt_scalef32_pk_bf16_fp4 v98, v82, 1.0
	v_cvt_scalef32_pk_bf16_fp4 v99, v82, 1.0 op_sel:[1,0,0]
	v_cvt_scalef32_pk_bf16_fp4 v100, v82, 1.0 op_sel:[0,1,0]
	v_cvt_scalef32_pk_bf16_fp4 v101, v82, 1.0 op_sel:[1,1,0]
	v_cvt_scalef32_pk_bf16_fp4 v102, v83, 1.0
	v_cvt_scalef32_pk_bf16_fp4 v103, v83, 1.0 op_sel:[1,0,0]
	v_cvt_scalef32_pk_bf16_fp4 v104, v83, 1.0 op_sel:[0,1,0]
	v_cvt_scalef32_pk_bf16_fp4 v105, v83, 1.0 op_sel:[1,1,0]
	v_mfma_f32_16x16x32_bf16 v[114:117], v[34:37], v[98:101], 0
	v_cvt_scalef32_pk_bf16_fp4 v98, v84, 1.0
	v_cvt_scalef32_pk_bf16_fp4 v99, v84, 1.0 op_sel:[1,0,0]
	v_cvt_scalef32_pk_bf16_fp4 v100, v84, 1.0 op_sel:[0,1,0]
	v_cvt_scalef32_pk_bf16_fp4 v101, v84, 1.0 op_sel:[1,1,0]
	v_mfma_f32_16x16x32_bf16 v[114:117], v[38:41], v[102:105], v[114:117]
	v_cvt_scalef32_pk_bf16_fp4 v102, v85, 1.0
	v_cvt_scalef32_pk_bf16_fp4 v103, v85, 1.0 op_sel:[1,0,0]
	v_cvt_scalef32_pk_bf16_fp4 v104, v85, 1.0 op_sel:[0,1,0]
	v_cvt_scalef32_pk_bf16_fp4 v105, v85, 1.0 op_sel:[1,1,0]
	v_mfma_f32_16x16x32_bf16 v[114:117], v[42:45], v[98:101], v[114:117]
	v_cvt_scalef32_pk_bf16_fp4 v98, v86, 1.0
	v_cvt_scalef32_pk_bf16_fp4 v99, v86, 1.0 op_sel:[1,0,0]
	v_cvt_scalef32_pk_bf16_fp4 v100, v86, 1.0 op_sel:[0,1,0]
	v_cvt_scalef32_pk_bf16_fp4 v101, v86, 1.0 op_sel:[1,1,0]
	v_mfma_f32_16x16x32_bf16 v[114:117], v[46:49], v[102:105], v[114:117]
	v_cvt_scalef32_pk_bf16_fp4 v102, v87, 1.0
	v_cvt_scalef32_pk_bf16_fp4 v103, v87, 1.0 op_sel:[1,0,0]
	v_cvt_scalef32_pk_bf16_fp4 v104, v87, 1.0 op_sel:[0,1,0]
	v_cvt_scalef32_pk_bf16_fp4 v105, v87, 1.0 op_sel:[1,1,0]
	v_mfma_f32_16x16x32_bf16 v[114:117], v[50:53], v[98:101], v[114:117]
	v_cvt_scalef32_pk_bf16_fp4 v98, v88, 1.0
	v_cvt_scalef32_pk_bf16_fp4 v99, v88, 1.0 op_sel:[1,0,0]
	v_cvt_scalef32_pk_bf16_fp4 v100, v88, 1.0 op_sel:[0,1,0]
	v_cvt_scalef32_pk_bf16_fp4 v101, v88, 1.0 op_sel:[1,1,0]
	v_mfma_f32_16x16x32_bf16 v[114:117], v[54:57], v[102:105], v[114:117]
	v_cvt_scalef32_pk_bf16_fp4 v102, v89, 1.0
	v_cvt_scalef32_pk_bf16_fp4 v103, v89, 1.0 op_sel:[1,0,0]
	v_cvt_scalef32_pk_bf16_fp4 v104, v89, 1.0 op_sel:[0,1,0]
	v_cvt_scalef32_pk_bf16_fp4 v105, v89, 1.0 op_sel:[1,1,0]
	v_mfma_f32_16x16x32_bf16 v[114:117], v[58:61], v[98:101], v[114:117]
	v_mfma_f32_16x16x32_bf16 v[114:117], v[62:65], v[102:105], v[114:117]
	s_waitcnt vmcnt(15)
	ds_read_b128 v[82:85], v146 offset:8192
	ds_read_b128 v[86:89], v147 offset:8192
	s_waitcnt lgkmcnt(2)
	s_add_i32 m0, s38, 0x1800
	v_mad_u32_u16 v142, v67, v249, v144 op_sel:[1,0,0,0]
	global_load_lds_dwordx4 v142, s[10:11]
	s_add_i32 m0, s38, 0x1c00
	v_mad_u32_u16 v143, v71, v249, v145 op_sel:[1,0,0,0]
	global_load_lds_dwordx4 v143, s[10:11]
	v_cvt_scalef32_pk_bf16_fp4 v98, v90, 1.0
	v_cvt_scalef32_pk_bf16_fp4 v99, v90, 1.0 op_sel:[1,0,0]
	v_cvt_scalef32_pk_bf16_fp4 v100, v90, 1.0 op_sel:[0,1,0]
	v_cvt_scalef32_pk_bf16_fp4 v101, v90, 1.0 op_sel:[1,1,0]
	v_cvt_scalef32_pk_bf16_fp4 v102, v91, 1.0
	v_cvt_scalef32_pk_bf16_fp4 v103, v91, 1.0 op_sel:[1,0,0]
	v_cvt_scalef32_pk_bf16_fp4 v104, v91, 1.0 op_sel:[0,1,0]
	v_cvt_scalef32_pk_bf16_fp4 v105, v91, 1.0 op_sel:[1,1,0]
	v_mfma_f32_16x16x32_bf16 v[118:121], v[34:37], v[98:101], 0
	v_cvt_scalef32_pk_bf16_fp4 v98, v92, 1.0
	v_cvt_scalef32_pk_bf16_fp4 v99, v92, 1.0 op_sel:[1,0,0]
	v_cvt_scalef32_pk_bf16_fp4 v100, v92, 1.0 op_sel:[0,1,0]
	v_cvt_scalef32_pk_bf16_fp4 v101, v92, 1.0 op_sel:[1,1,0]
	v_mfma_f32_16x16x32_bf16 v[118:121], v[38:41], v[102:105], v[118:121]
	v_cvt_scalef32_pk_bf16_fp4 v102, v93, 1.0
	v_cvt_scalef32_pk_bf16_fp4 v103, v93, 1.0 op_sel:[1,0,0]
	v_cvt_scalef32_pk_bf16_fp4 v104, v93, 1.0 op_sel:[0,1,0]
	v_cvt_scalef32_pk_bf16_fp4 v105, v93, 1.0 op_sel:[1,1,0]
	v_mfma_f32_16x16x32_bf16 v[118:121], v[42:45], v[98:101], v[118:121]
	v_cvt_scalef32_pk_bf16_fp4 v98, v94, 1.0
	v_cvt_scalef32_pk_bf16_fp4 v99, v94, 1.0 op_sel:[1,0,0]
	v_cvt_scalef32_pk_bf16_fp4 v100, v94, 1.0 op_sel:[0,1,0]
	v_cvt_scalef32_pk_bf16_fp4 v101, v94, 1.0 op_sel:[1,1,0]
	v_mfma_f32_16x16x32_bf16 v[118:121], v[46:49], v[102:105], v[118:121]
	v_cvt_scalef32_pk_bf16_fp4 v102, v95, 1.0
	v_cvt_scalef32_pk_bf16_fp4 v103, v95, 1.0 op_sel:[1,0,0]
	v_cvt_scalef32_pk_bf16_fp4 v104, v95, 1.0 op_sel:[0,1,0]
	v_cvt_scalef32_pk_bf16_fp4 v105, v95, 1.0 op_sel:[1,1,0]
	v_mfma_f32_16x16x32_bf16 v[118:121], v[50:53], v[98:101], v[118:121]
	v_cvt_scalef32_pk_bf16_fp4 v98, v96, 1.0
	v_cvt_scalef32_pk_bf16_fp4 v99, v96, 1.0 op_sel:[1,0,0]
	v_cvt_scalef32_pk_bf16_fp4 v100, v96, 1.0 op_sel:[0,1,0]
	v_cvt_scalef32_pk_bf16_fp4 v101, v96, 1.0 op_sel:[1,1,0]
	v_mfma_f32_16x16x32_bf16 v[118:121], v[54:57], v[102:105], v[118:121]
	v_cvt_scalef32_pk_bf16_fp4 v102, v97, 1.0
	v_cvt_scalef32_pk_bf16_fp4 v103, v97, 1.0 op_sel:[1,0,0]
	v_cvt_scalef32_pk_bf16_fp4 v104, v97, 1.0 op_sel:[0,1,0]
	v_cvt_scalef32_pk_bf16_fp4 v105, v97, 1.0 op_sel:[1,1,0]
	v_mfma_f32_16x16x32_bf16 v[118:121], v[58:61], v[98:101], v[118:121]
	v_cvt_pk_bf16_f32 v138, v106, v110
	v_mfma_f32_16x16x32_bf16 v[118:121], v[62:65], v[102:105], v[118:121]
	s_waitcnt vmcnt(15)
	ds_read_b128 v[90:93], v146 offset:10240
	ds_read_b128 v[94:97], v147 offset:10240
	s_waitcnt lgkmcnt(2)
	s_add_i32 m0, s38, 0x2000
	v_mad_u32_u16 v142, v68, v249, v144
	global_load_lds_dwordx4 v142, s[10:11]
	s_add_i32 m0, s38, 0x2400
	v_mad_u32_u16 v143, v72, v249, v145
	global_load_lds_dwordx4 v143, s[10:11]
	v_cvt_scalef32_pk_bf16_fp4 v98, v82, 1.0
	v_cvt_scalef32_pk_bf16_fp4 v99, v82, 1.0 op_sel:[1,0,0]
	v_cvt_scalef32_pk_bf16_fp4 v100, v82, 1.0 op_sel:[0,1,0]
	v_cvt_scalef32_pk_bf16_fp4 v101, v82, 1.0 op_sel:[1,1,0]
	v_cvt_scalef32_pk_bf16_fp4 v102, v83, 1.0
	v_cvt_scalef32_pk_bf16_fp4 v103, v83, 1.0 op_sel:[1,0,0]
	v_cvt_scalef32_pk_bf16_fp4 v104, v83, 1.0 op_sel:[0,1,0]
	v_cvt_scalef32_pk_bf16_fp4 v105, v83, 1.0 op_sel:[1,1,0]
	v_mfma_f32_16x16x32_bf16 v[122:125], v[34:37], v[98:101], 0
	v_cvt_scalef32_pk_bf16_fp4 v98, v84, 1.0
	v_cvt_scalef32_pk_bf16_fp4 v99, v84, 1.0 op_sel:[1,0,0]
	v_cvt_scalef32_pk_bf16_fp4 v100, v84, 1.0 op_sel:[0,1,0]
	v_cvt_scalef32_pk_bf16_fp4 v101, v84, 1.0 op_sel:[1,1,0]
	v_mfma_f32_16x16x32_bf16 v[122:125], v[38:41], v[102:105], v[122:125]
	v_cvt_scalef32_pk_bf16_fp4 v102, v85, 1.0
	v_cvt_scalef32_pk_bf16_fp4 v103, v85, 1.0 op_sel:[1,0,0]
	v_cvt_scalef32_pk_bf16_fp4 v104, v85, 1.0 op_sel:[0,1,0]
	v_cvt_scalef32_pk_bf16_fp4 v105, v85, 1.0 op_sel:[1,1,0]
	v_mfma_f32_16x16x32_bf16 v[122:125], v[42:45], v[98:101], v[122:125]
	v_cvt_scalef32_pk_bf16_fp4 v98, v86, 1.0
	v_cvt_scalef32_pk_bf16_fp4 v99, v86, 1.0 op_sel:[1,0,0]
	v_cvt_scalef32_pk_bf16_fp4 v100, v86, 1.0 op_sel:[0,1,0]
	v_cvt_scalef32_pk_bf16_fp4 v101, v86, 1.0 op_sel:[1,1,0]
	v_mfma_f32_16x16x32_bf16 v[122:125], v[46:49], v[102:105], v[122:125]
	v_cvt_scalef32_pk_bf16_fp4 v102, v87, 1.0
	v_cvt_scalef32_pk_bf16_fp4 v103, v87, 1.0 op_sel:[1,0,0]
	v_cvt_scalef32_pk_bf16_fp4 v104, v87, 1.0 op_sel:[0,1,0]
	v_cvt_scalef32_pk_bf16_fp4 v105, v87, 1.0 op_sel:[1,1,0]
	v_mfma_f32_16x16x32_bf16 v[122:125], v[50:53], v[98:101], v[122:125]
	v_cvt_scalef32_pk_bf16_fp4 v98, v88, 1.0
	v_cvt_scalef32_pk_bf16_fp4 v99, v88, 1.0 op_sel:[1,0,0]
	v_cvt_scalef32_pk_bf16_fp4 v100, v88, 1.0 op_sel:[0,1,0]
	v_cvt_scalef32_pk_bf16_fp4 v101, v88, 1.0 op_sel:[1,1,0]
	v_mfma_f32_16x16x32_bf16 v[122:125], v[54:57], v[102:105], v[122:125]
	v_cvt_scalef32_pk_bf16_fp4 v102, v89, 1.0
	v_cvt_scalef32_pk_bf16_fp4 v103, v89, 1.0 op_sel:[1,0,0]
	v_cvt_scalef32_pk_bf16_fp4 v104, v89, 1.0 op_sel:[0,1,0]
	v_cvt_scalef32_pk_bf16_fp4 v105, v89, 1.0 op_sel:[1,1,0]
	v_mfma_f32_16x16x32_bf16 v[122:125], v[58:61], v[98:101], v[122:125]
	v_mfma_f32_16x16x32_bf16 v[122:125], v[62:65], v[102:105], v[122:125]
	s_waitcnt vmcnt(15)
	ds_read_b128 v[82:85], v146 offset:12288
	ds_read_b128 v[86:89], v147 offset:12288
	s_waitcnt lgkmcnt(2)
	s_add_i32 m0, s38, 0x2800
	v_mad_u32_u16 v142, v68, v249, v144 op_sel:[1,0,0,0]
	global_load_lds_dwordx4 v142, s[10:11]
	s_add_i32 m0, s38, 0x2c00
	v_mad_u32_u16 v143, v72, v249, v145 op_sel:[1,0,0,0]
	global_load_lds_dwordx4 v143, s[10:11]
	v_cvt_scalef32_pk_bf16_fp4 v98, v90, 1.0
	v_cvt_scalef32_pk_bf16_fp4 v99, v90, 1.0 op_sel:[1,0,0]
	v_cvt_scalef32_pk_bf16_fp4 v100, v90, 1.0 op_sel:[0,1,0]
	v_cvt_scalef32_pk_bf16_fp4 v101, v90, 1.0 op_sel:[1,1,0]
	v_cvt_scalef32_pk_bf16_fp4 v102, v91, 1.0
	v_cvt_scalef32_pk_bf16_fp4 v103, v91, 1.0 op_sel:[1,0,0]
	v_cvt_scalef32_pk_bf16_fp4 v104, v91, 1.0 op_sel:[0,1,0]
	v_cvt_scalef32_pk_bf16_fp4 v105, v91, 1.0 op_sel:[1,1,0]
	v_mfma_f32_16x16x32_bf16 v[126:129], v[34:37], v[98:101], 0
	v_cvt_scalef32_pk_bf16_fp4 v98, v92, 1.0
	v_cvt_scalef32_pk_bf16_fp4 v99, v92, 1.0 op_sel:[1,0,0]
	v_cvt_scalef32_pk_bf16_fp4 v100, v92, 1.0 op_sel:[0,1,0]
	v_cvt_scalef32_pk_bf16_fp4 v101, v92, 1.0 op_sel:[1,1,0]
	v_mfma_f32_16x16x32_bf16 v[126:129], v[38:41], v[102:105], v[126:129]
	v_cvt_scalef32_pk_bf16_fp4 v102, v93, 1.0
	v_cvt_scalef32_pk_bf16_fp4 v103, v93, 1.0 op_sel:[1,0,0]
	v_cvt_scalef32_pk_bf16_fp4 v104, v93, 1.0 op_sel:[0,1,0]
	v_cvt_scalef32_pk_bf16_fp4 v105, v93, 1.0 op_sel:[1,1,0]
	v_mfma_f32_16x16x32_bf16 v[126:129], v[42:45], v[98:101], v[126:129]
	v_cvt_scalef32_pk_bf16_fp4 v98, v94, 1.0
	v_cvt_scalef32_pk_bf16_fp4 v99, v94, 1.0 op_sel:[1,0,0]
	v_cvt_scalef32_pk_bf16_fp4 v100, v94, 1.0 op_sel:[0,1,0]
	v_cvt_scalef32_pk_bf16_fp4 v101, v94, 1.0 op_sel:[1,1,0]
	v_mfma_f32_16x16x32_bf16 v[126:129], v[46:49], v[102:105], v[126:129]
	v_cvt_scalef32_pk_bf16_fp4 v102, v95, 1.0
	v_cvt_scalef32_pk_bf16_fp4 v103, v95, 1.0 op_sel:[1,0,0]
	v_cvt_scalef32_pk_bf16_fp4 v104, v95, 1.0 op_sel:[0,1,0]
	v_cvt_scalef32_pk_bf16_fp4 v105, v95, 1.0 op_sel:[1,1,0]
	v_mfma_f32_16x16x32_bf16 v[126:129], v[50:53], v[98:101], v[126:129]
	v_cvt_scalef32_pk_bf16_fp4 v98, v96, 1.0
	v_cvt_scalef32_pk_bf16_fp4 v99, v96, 1.0 op_sel:[1,0,0]
	v_cvt_scalef32_pk_bf16_fp4 v100, v96, 1.0 op_sel:[0,1,0]
	v_cvt_scalef32_pk_bf16_fp4 v101, v96, 1.0 op_sel:[1,1,0]
	v_mfma_f32_16x16x32_bf16 v[126:129], v[54:57], v[102:105], v[126:129]
	v_cvt_scalef32_pk_bf16_fp4 v102, v97, 1.0
	v_cvt_scalef32_pk_bf16_fp4 v103, v97, 1.0 op_sel:[1,0,0]
	v_cvt_scalef32_pk_bf16_fp4 v104, v97, 1.0 op_sel:[0,1,0]
	v_cvt_scalef32_pk_bf16_fp4 v105, v97, 1.0 op_sel:[1,1,0]
	v_mfma_f32_16x16x32_bf16 v[126:129], v[58:61], v[98:101], v[126:129]
	v_cvt_pk_bf16_f32 v139, v114, v118
	v_mfma_f32_16x16x32_bf16 v[126:129], v[62:65], v[102:105], v[126:129]
	s_waitcnt vmcnt(15)
	ds_read_b128 v[90:93], v146 offset:14336
	ds_read_b128 v[94:97], v147 offset:14336
	s_waitcnt lgkmcnt(2)
	s_add_i32 m0, s38, 0x3000
	v_mad_u32_u16 v142, v69, v249, v144
	global_load_lds_dwordx4 v142, s[10:11]
	s_add_i32 m0, s38, 0x3400
	v_mad_u32_u16 v143, v73, v249, v145
	global_load_lds_dwordx4 v143, s[10:11]
	v_cvt_scalef32_pk_bf16_fp4 v98, v82, 1.0
	v_cvt_scalef32_pk_bf16_fp4 v99, v82, 1.0 op_sel:[1,0,0]
	v_cvt_scalef32_pk_bf16_fp4 v100, v82, 1.0 op_sel:[0,1,0]
	v_cvt_scalef32_pk_bf16_fp4 v101, v82, 1.0 op_sel:[1,1,0]
	v_cvt_scalef32_pk_bf16_fp4 v102, v83, 1.0
	v_cvt_scalef32_pk_bf16_fp4 v103, v83, 1.0 op_sel:[1,0,0]
	v_cvt_scalef32_pk_bf16_fp4 v104, v83, 1.0 op_sel:[0,1,0]
	v_cvt_scalef32_pk_bf16_fp4 v105, v83, 1.0 op_sel:[1,1,0]
	v_mfma_f32_16x16x32_bf16 v[130:133], v[34:37], v[98:101], 0
	v_cvt_scalef32_pk_bf16_fp4 v98, v84, 1.0
	v_cvt_scalef32_pk_bf16_fp4 v99, v84, 1.0 op_sel:[1,0,0]
	v_cvt_scalef32_pk_bf16_fp4 v100, v84, 1.0 op_sel:[0,1,0]
	v_cvt_scalef32_pk_bf16_fp4 v101, v84, 1.0 op_sel:[1,1,0]
	v_mfma_f32_16x16x32_bf16 v[130:133], v[38:41], v[102:105], v[130:133]
	v_cvt_scalef32_pk_bf16_fp4 v102, v85, 1.0
	v_cvt_scalef32_pk_bf16_fp4 v103, v85, 1.0 op_sel:[1,0,0]
	v_cvt_scalef32_pk_bf16_fp4 v104, v85, 1.0 op_sel:[0,1,0]
	v_cvt_scalef32_pk_bf16_fp4 v105, v85, 1.0 op_sel:[1,1,0]
	v_mfma_f32_16x16x32_bf16 v[130:133], v[42:45], v[98:101], v[130:133]
	v_cvt_scalef32_pk_bf16_fp4 v98, v86, 1.0
	v_cvt_scalef32_pk_bf16_fp4 v99, v86, 1.0 op_sel:[1,0,0]
	v_cvt_scalef32_pk_bf16_fp4 v100, v86, 1.0 op_sel:[0,1,0]
	v_cvt_scalef32_pk_bf16_fp4 v101, v86, 1.0 op_sel:[1,1,0]
	v_mfma_f32_16x16x32_bf16 v[130:133], v[46:49], v[102:105], v[130:133]
	v_cvt_scalef32_pk_bf16_fp4 v102, v87, 1.0
	v_cvt_scalef32_pk_bf16_fp4 v103, v87, 1.0 op_sel:[1,0,0]
	v_cvt_scalef32_pk_bf16_fp4 v104, v87, 1.0 op_sel:[0,1,0]
	v_cvt_scalef32_pk_bf16_fp4 v105, v87, 1.0 op_sel:[1,1,0]
	v_mfma_f32_16x16x32_bf16 v[130:133], v[50:53], v[98:101], v[130:133]
	v_cvt_scalef32_pk_bf16_fp4 v98, v88, 1.0
	v_cvt_scalef32_pk_bf16_fp4 v99, v88, 1.0 op_sel:[1,0,0]
	v_cvt_scalef32_pk_bf16_fp4 v100, v88, 1.0 op_sel:[0,1,0]
	v_cvt_scalef32_pk_bf16_fp4 v101, v88, 1.0 op_sel:[1,1,0]
	v_mfma_f32_16x16x32_bf16 v[130:133], v[54:57], v[102:105], v[130:133]
	v_cvt_scalef32_pk_bf16_fp4 v102, v89, 1.0
	v_cvt_scalef32_pk_bf16_fp4 v103, v89, 1.0 op_sel:[1,0,0]
	v_cvt_scalef32_pk_bf16_fp4 v104, v89, 1.0 op_sel:[0,1,0]
	v_cvt_scalef32_pk_bf16_fp4 v105, v89, 1.0 op_sel:[1,1,0]
	v_mfma_f32_16x16x32_bf16 v[130:133], v[58:61], v[98:101], v[130:133]
	v_mfma_f32_16x16x32_bf16 v[130:133], v[62:65], v[102:105], v[130:133]
	s_waitcnt vmcnt(12)
	ds_read_b128 v[82:85], v146
	ds_read_b128 v[86:89], v147
	s_waitcnt lgkmcnt(2)
	s_add_i32 m0, s38, 0x3800
	v_mad_u32_u16 v142, v69, v249, v144 op_sel:[1,0,0,0]
	global_load_lds_dwordx4 v142, s[10:11]
	s_add_i32 m0, s38, 0x3c00
	v_mad_u32_u16 v143, v73, v249, v145 op_sel:[1,0,0,0]
	global_load_lds_dwordx4 v143, s[10:11]
	ds_read_b128 v[2:5], v148
	ds_read_b128 v[6:9], v148 offset:16
	ds_read_b128 v[10:13], v148 offset:32
	ds_read_b128 v[14:17], v148 offset:48
	ds_read_b128 v[18:21], v148 offset:256
	ds_read_b128 v[22:25], v148 offset:272
	ds_read_b128 v[26:29], v148 offset:288
	ds_read_b128 v[30:33], v148 offset:304
	ds_read_b128 v[74:77], v152 offset:256
	ds_read_b128 v[78:81], v152 offset:272
	v_cvt_scalef32_pk_bf16_fp4 v98, v90, 1.0
	v_cvt_scalef32_pk_bf16_fp4 v99, v90, 1.0 op_sel:[1,0,0]
	v_cvt_scalef32_pk_bf16_fp4 v100, v90, 1.0 op_sel:[0,1,0]
	v_cvt_scalef32_pk_bf16_fp4 v101, v90, 1.0 op_sel:[1,1,0]
	v_cvt_scalef32_pk_bf16_fp4 v102, v91, 1.0
	v_cvt_scalef32_pk_bf16_fp4 v103, v91, 1.0 op_sel:[1,0,0]
	v_cvt_scalef32_pk_bf16_fp4 v104, v91, 1.0 op_sel:[0,1,0]
	v_cvt_scalef32_pk_bf16_fp4 v105, v91, 1.0 op_sel:[1,1,0]
	v_mfma_f32_16x16x32_bf16 v[134:137], v[34:37], v[98:101], 0
	v_cvt_scalef32_pk_bf16_fp4 v98, v92, 1.0
	v_cvt_scalef32_pk_bf16_fp4 v99, v92, 1.0 op_sel:[1,0,0]
	v_cvt_scalef32_pk_bf16_fp4 v100, v92, 1.0 op_sel:[0,1,0]
	v_cvt_scalef32_pk_bf16_fp4 v101, v92, 1.0 op_sel:[1,1,0]
	v_mfma_f32_16x16x32_bf16 v[134:137], v[38:41], v[102:105], v[134:137]
	v_cvt_scalef32_pk_bf16_fp4 v102, v93, 1.0
	v_cvt_scalef32_pk_bf16_fp4 v103, v93, 1.0 op_sel:[1,0,0]
	v_cvt_scalef32_pk_bf16_fp4 v104, v93, 1.0 op_sel:[0,1,0]
	v_cvt_scalef32_pk_bf16_fp4 v105, v93, 1.0 op_sel:[1,1,0]
	v_mfma_f32_16x16x32_bf16 v[134:137], v[42:45], v[98:101], v[134:137]
	v_cvt_scalef32_pk_bf16_fp4 v98, v94, 1.0
	v_cvt_scalef32_pk_bf16_fp4 v99, v94, 1.0 op_sel:[1,0,0]
	v_cvt_scalef32_pk_bf16_fp4 v100, v94, 1.0 op_sel:[0,1,0]
	v_cvt_scalef32_pk_bf16_fp4 v101, v94, 1.0 op_sel:[1,1,0]
	v_mfma_f32_16x16x32_bf16 v[134:137], v[46:49], v[102:105], v[134:137]
	v_cvt_scalef32_pk_bf16_fp4 v102, v95, 1.0
	v_cvt_scalef32_pk_bf16_fp4 v103, v95, 1.0 op_sel:[1,0,0]
	v_cvt_scalef32_pk_bf16_fp4 v104, v95, 1.0 op_sel:[0,1,0]
	v_cvt_scalef32_pk_bf16_fp4 v105, v95, 1.0 op_sel:[1,1,0]
	v_mfma_f32_16x16x32_bf16 v[134:137], v[50:53], v[98:101], v[134:137]
	v_cvt_scalef32_pk_bf16_fp4 v98, v96, 1.0
	v_cvt_scalef32_pk_bf16_fp4 v99, v96, 1.0 op_sel:[1,0,0]
	v_cvt_scalef32_pk_bf16_fp4 v100, v96, 1.0 op_sel:[0,1,0]
	v_cvt_scalef32_pk_bf16_fp4 v101, v96, 1.0 op_sel:[1,1,0]
	v_mfma_f32_16x16x32_bf16 v[134:137], v[54:57], v[102:105], v[134:137]
	v_cvt_scalef32_pk_bf16_fp4 v102, v97, 1.0
	v_cvt_scalef32_pk_bf16_fp4 v103, v97, 1.0 op_sel:[1,0,0]
	v_cvt_scalef32_pk_bf16_fp4 v104, v97, 1.0 op_sel:[0,1,0]
	v_cvt_scalef32_pk_bf16_fp4 v105, v97, 1.0 op_sel:[1,1,0]
	v_mfma_f32_16x16x32_bf16 v[134:137], v[58:61], v[98:101], v[134:137]
	v_cvt_pk_bf16_f32 v140, v122, v126
	v_mfma_f32_16x16x32_bf16 v[134:137], v[62:65], v[102:105], v[134:137]
	s_nop 7
	v_cvt_pk_bf16_f32 v141, v130, v134
	s_mov_b64 exec, 0xffff
	global_store_dwordx4 v151, v[138:141], s[4:5]
	s_mov_b64 exec, -1
	v_add_u32_e32 v151, s42, v151
	s_add_i32 s34, s34, 2
	s_cmp_lt_u32 s34, 8
	s_cbranch_scc1 .Le1_loop
	s_cmp_lt_i32 s35, 0
	s_cbranch_scc1 .Le1_exit
	s_add_i32 s39, s39, s43
	s_add_i32 s39, s39, 7
	s_mov_b32 s34, 0
	s_branch .Le1_loop

.Le2_noprep:
	s_lshr_b32 s99, s38, 4
	s_add_i32 m0, s99, 0x21100
	s_mov_b64 exec, 0xffff
	global_load_lds_dwordx4 v177, s[0:1]
	s_mov_b64 exec, -1
	s_lshl_b32 s99, s43, 8
	s_cmp_eq_u32 s33, 6
	s_cselect_b32 s99, s99, 0x100
	v_add_u32_e32 v177, s99, v177
	s_lshr_b32 s99, s38, 5
	s_add_i32 m0, s99, 0x23000
	s_mov_b64 exec, 0xffff
	global_load_lds_dwordx4 v176, s[22:23]
	s_mov_b64 exec, -1
	v_add_u32_e32 v176, 0x100, v176
	global_load_dword v130, v[180:181], off
	global_load_dword v131, v[180:181], off offset:256
	global_load_dword v132, v[180:181], off offset:512
	global_load_dword v133, v[180:181], off offset:768
	ds_read_b64_tr_b4 v[118:119], v151
	ds_read_b64_tr_b4 v[120:121], v159
	s_waitcnt lgkmcnt(2)
	v_cvt_scalef32_pk_f16_fp4 v122, v114, 1.0
	v_cvt_scalef32_pk_f16_fp4 v123, v114, 1.0 op_sel:[1,0,0]
	v_cvt_scalef32_pk_f16_fp4 v124, v114, 1.0 op_sel:[0,1,0]
	v_cvt_scalef32_pk_f16_fp4 v125, v114, 1.0 op_sel:[1,1,0]
	v_cvt_scalef32_pk_f16_fp4 v126, v116, 1.0
	v_cvt_scalef32_pk_f16_fp4 v127, v116, 1.0 op_sel:[1,0,0]
	v_cvt_scalef32_pk_f16_fp4 v128, v116, 1.0 op_sel:[0,1,0]
	v_cvt_scalef32_pk_f16_fp4 v129, v116, 1.0 op_sel:[1,1,0]
	v_mfma_f32_16x16x32_f16 v[2:5], v[66:69], v[122:125], 0
	v_cvt_scalef32_pk_f16_fp4 v122, v117, 1.0
	v_cvt_scalef32_pk_f16_fp4 v123, v117, 1.0 op_sel:[1,0,0]
	v_cvt_scalef32_pk_f16_fp4 v124, v117, 1.0 op_sel:[0,1,0]
	v_cvt_scalef32_pk_f16_fp4 v125, v117, 1.0 op_sel:[1,1,0]
	v_mfma_f32_16x16x32_f16 v[6:9], v[66:69], v[126:129], 0
	v_cvt_scalef32_pk_f16_fp4 v126, v115, 1.0
	v_cvt_scalef32_pk_f16_fp4 v127, v115, 1.0 op_sel:[1,0,0]
	v_cvt_scalef32_pk_f16_fp4 v128, v115, 1.0 op_sel:[0,1,0]
	v_cvt_scalef32_pk_f16_fp4 v129, v115, 1.0 op_sel:[1,1,0]
	v_mfma_f32_16x16x32_f16 v[2:5], v[74:77], v[122:125], v[2:5]
	v_mfma_f32_16x16x32_f16 v[6:9], v[74:77], v[126:129], v[6:9]
	ds_read_b64_tr_b4 v[114:115], v152
	ds_read_b64_tr_b4 v[116:117], v160
	s_waitcnt lgkmcnt(2)
	v_cvt_scalef32_pk_f16_fp4 v122, v118, 1.0
	v_cvt_scalef32_pk_f16_fp4 v123, v118, 1.0 op_sel:[1,0,0]
	v_cvt_scalef32_pk_f16_fp4 v124, v118, 1.0 op_sel:[0,1,0]
	v_cvt_scalef32_pk_f16_fp4 v125, v118, 1.0 op_sel:[1,1,0]
	v_cvt_scalef32_pk_f16_fp4 v126, v120, 1.0
	v_cvt_scalef32_pk_f16_fp4 v127, v120, 1.0 op_sel:[1,0,0]
	v_cvt_scalef32_pk_f16_fp4 v128, v120, 1.0 op_sel:[0,1,0]
	v_cvt_scalef32_pk_f16_fp4 v129, v120, 1.0 op_sel:[1,1,0]
	v_mfma_f32_16x16x32_f16 v[10:13], v[66:69], v[122:125], 0
	v_cvt_scalef32_pk_f16_fp4 v122, v121, 1.0
	v_cvt_scalef32_pk_f16_fp4 v123, v121, 1.0 op_sel:[1,0,0]
	v_cvt_scalef32_pk_f16_fp4 v124, v121, 1.0 op_sel:[0,1,0]
	v_cvt_scalef32_pk_f16_fp4 v125, v121, 1.0 op_sel:[1,1,0]
	v_mfma_f32_16x16x32_f16 v[14:17], v[66:69], v[126:129], 0
	v_cvt_scalef32_pk_f16_fp4 v126, v119, 1.0
	v_cvt_scalef32_pk_f16_fp4 v127, v119, 1.0 op_sel:[1,0,0]
	v_cvt_scalef32_pk_f16_fp4 v128, v119, 1.0 op_sel:[0,1,0]
	v_cvt_scalef32_pk_f16_fp4 v129, v119, 1.0 op_sel:[1,1,0]
	v_mfma_f32_16x16x32_f16 v[10:13], v[74:77], v[122:125], v[10:13]
	v_mfma_f32_16x16x32_f16 v[14:17], v[74:77], v[126:129], v[14:17]
	ds_read_b64_tr_b4 v[118:119], v153
	ds_read_b64_tr_b4 v[120:121], v161
	s_waitcnt lgkmcnt(2)
	v_cvt_scalef32_pk_f16_fp4 v122, v114, 1.0
	v_cvt_scalef32_pk_f16_fp4 v123, v114, 1.0 op_sel:[1,0,0]
	v_cvt_scalef32_pk_f16_fp4 v124, v114, 1.0 op_sel:[0,1,0]
	v_cvt_scalef32_pk_f16_fp4 v125, v114, 1.0 op_sel:[1,1,0]
	v_cvt_scalef32_pk_f16_fp4 v126, v116, 1.0
	v_cvt_scalef32_pk_f16_fp4 v127, v116, 1.0 op_sel:[1,0,0]
	v_cvt_scalef32_pk_f16_fp4 v128, v116, 1.0 op_sel:[0,1,0]
	v_cvt_scalef32_pk_f16_fp4 v129, v116, 1.0 op_sel:[1,1,0]
	v_mfma_f32_16x16x32_f16 v[18:21], v[66:69], v[122:125], 0
	v_cvt_scalef32_pk_f16_fp4 v122, v117, 1.0
	v_cvt_scalef32_pk_f16_fp4 v123, v117, 1.0 op_sel:[1,0,0]
	v_cvt_scalef32_pk_f16_fp4 v124, v117, 1.0 op_sel:[0,1,0]
	v_cvt_scalef32_pk_f16_fp4 v125, v117, 1.0 op_sel:[1,1,0]
	v_mfma_f32_16x16x32_f16 v[22:25], v[66:69], v[126:129], 0
	v_cvt_scalef32_pk_f16_fp4 v126, v115, 1.0
	v_cvt_scalef32_pk_f16_fp4 v127, v115, 1.0 op_sel:[1,0,0]
	v_cvt_scalef32_pk_f16_fp4 v128, v115, 1.0 op_sel:[0,1,0]
	v_cvt_scalef32_pk_f16_fp4 v129, v115, 1.0 op_sel:[1,1,0]
	v_mfma_f32_16x16x32_f16 v[18:21], v[74:77], v[122:125], v[18:21]
	v_mfma_f32_16x16x32_f16 v[22:25], v[74:77], v[126:129], v[22:25]
	ds_read_b64_tr_b4 v[114:115], v154
	ds_read_b64_tr_b4 v[116:117], v162
	s_waitcnt lgkmcnt(2)
	v_cvt_scalef32_pk_f16_fp4 v122, v118, 1.0
	v_cvt_scalef32_pk_f16_fp4 v123, v118, 1.0 op_sel:[1,0,0]
	v_cvt_scalef32_pk_f16_fp4 v124, v118, 1.0 op_sel:[0,1,0]
	v_cvt_scalef32_pk_f16_fp4 v125, v118, 1.0 op_sel:[1,1,0]
	v_cvt_scalef32_pk_f16_fp4 v126, v120, 1.0
	v_cvt_scalef32_pk_f16_fp4 v127, v120, 1.0 op_sel:[1,0,0]
	v_cvt_scalef32_pk_f16_fp4 v128, v120, 1.0 op_sel:[0,1,0]
	v_cvt_scalef32_pk_f16_fp4 v129, v120, 1.0 op_sel:[1,1,0]
	v_mfma_f32_16x16x32_f16 v[26:29], v[66:69], v[122:125], 0
	v_cvt_scalef32_pk_f16_fp4 v122, v121, 1.0
	v_cvt_scalef32_pk_f16_fp4 v123, v121, 1.0 op_sel:[1,0,0]
	v_cvt_scalef32_pk_f16_fp4 v124, v121, 1.0 op_sel:[0,1,0]
	v_cvt_scalef32_pk_f16_fp4 v125, v121, 1.0 op_sel:[1,1,0]
	v_mfma_f32_16x16x32_f16 v[30:33], v[66:69], v[126:129], 0
	v_cvt_scalef32_pk_f16_fp4 v126, v119, 1.0
	v_cvt_scalef32_pk_f16_fp4 v127, v119, 1.0 op_sel:[1,0,0]
	v_cvt_scalef32_pk_f16_fp4 v128, v119, 1.0 op_sel:[0,1,0]
	v_cvt_scalef32_pk_f16_fp4 v129, v119, 1.0 op_sel:[1,1,0]
	v_mfma_f32_16x16x32_f16 v[26:29], v[74:77], v[122:125], v[26:29]
	v_mfma_f32_16x16x32_f16 v[30:33], v[74:77], v[126:129], v[30:33]
	ds_read_b64_tr_b4 v[118:119], v155
	ds_read_b64_tr_b4 v[120:121], v163
	s_waitcnt lgkmcnt(2)
	v_cvt_scalef32_pk_f16_fp4 v122, v114, 1.0
	v_cvt_scalef32_pk_f16_fp4 v123, v114, 1.0 op_sel:[1,0,0]
	v_cvt_scalef32_pk_f16_fp4 v124, v114, 1.0 op_sel:[0,1,0]
	v_cvt_scalef32_pk_f16_fp4 v125, v114, 1.0 op_sel:[1,1,0]
	v_cvt_scalef32_pk_f16_fp4 v126, v116, 1.0
	v_cvt_scalef32_pk_f16_fp4 v127, v116, 1.0 op_sel:[1,0,0]
	v_cvt_scalef32_pk_f16_fp4 v128, v116, 1.0 op_sel:[0,1,0]
	v_cvt_scalef32_pk_f16_fp4 v129, v116, 1.0 op_sel:[1,1,0]
	v_mfma_f32_16x16x32_f16 v[34:37], v[66:69], v[122:125], 0
	v_cvt_scalef32_pk_f16_fp4 v122, v117, 1.0
	v_cvt_scalef32_pk_f16_fp4 v123, v117, 1.0 op_sel:[1,0,0]
	v_cvt_scalef32_pk_f16_fp4 v124, v117, 1.0 op_sel:[0,1,0]
	v_cvt_scalef32_pk_f16_fp4 v125, v117, 1.0 op_sel:[1,1,0]
	v_mfma_f32_16x16x32_f16 v[38:41], v[66:69], v[126:129], 0
	v_cvt_scalef32_pk_f16_fp4 v126, v115, 1.0
	v_cvt_scalef32_pk_f16_fp4 v127, v115, 1.0 op_sel:[1,0,0]
	v_cvt_scalef32_pk_f16_fp4 v128, v115, 1.0 op_sel:[0,1,0]
	v_cvt_scalef32_pk_f16_fp4 v129, v115, 1.0 op_sel:[1,1,0]
	v_mfma_f32_16x16x32_f16 v[34:37], v[74:77], v[122:125], v[34:37]
	v_mfma_f32_16x16x32_f16 v[38:41], v[74:77], v[126:129], v[38:41]
	ds_read_b64_tr_b4 v[114:115], v156
	ds_read_b64_tr_b4 v[116:117], v164
	s_waitcnt lgkmcnt(2)
	v_cvt_scalef32_pk_f16_fp4 v122, v118, 1.0
	v_cvt_scalef32_pk_f16_fp4 v123, v118, 1.0 op_sel:[1,0,0]
	v_cvt_scalef32_pk_f16_fp4 v124, v118, 1.0 op_sel:[0,1,0]
	v_cvt_scalef32_pk_f16_fp4 v125, v118, 1.0 op_sel:[1,1,0]
	v_cvt_scalef32_pk_f16_fp4 v126, v120, 1.0
	v_cvt_scalef32_pk_f16_fp4 v127, v120, 1.0 op_sel:[1,0,0]
	v_cvt_scalef32_pk_f16_fp4 v128, v120, 1.0 op_sel:[0,1,0]
	v_cvt_scalef32_pk_f16_fp4 v129, v120, 1.0 op_sel:[1,1,0]
	v_mfma_f32_16x16x32_f16 v[42:45], v[66:69], v[122:125], 0
	v_cvt_scalef32_pk_f16_fp4 v122, v121, 1.0
	v_cvt_scalef32_pk_f16_fp4 v123, v121, 1.0 op_sel:[1,0,0]
	v_cvt_scalef32_pk_f16_fp4 v124, v121, 1.0 op_sel:[0,1,0]
	v_cvt_scalef32_pk_f16_fp4 v125, v121, 1.0 op_sel:[1,1,0]
	v_mfma_f32_16x16x32_f16 v[46:49], v[66:69], v[126:129], 0
	v_cvt_scalef32_pk_f16_fp4 v126, v119, 1.0
	v_cvt_scalef32_pk_f16_fp4 v127, v119, 1.0 op_sel:[1,0,0]
	v_cvt_scalef32_pk_f16_fp4 v128, v119, 1.0 op_sel:[0,1,0]
	v_cvt_scalef32_pk_f16_fp4 v129, v119, 1.0 op_sel:[1,1,0]
	v_mfma_f32_16x16x32_f16 v[42:45], v[74:77], v[122:125], v[42:45]
	v_mfma_f32_16x16x32_f16 v[46:49], v[74:77], v[126:129], v[46:49]
	ds_read_b64_tr_b4 v[118:119], v157
	ds_read_b64_tr_b4 v[120:121], v165
	s_waitcnt lgkmcnt(2)
	v_cvt_scalef32_pk_f16_fp4 v122, v114, 1.0
	v_cvt_scalef32_pk_f16_fp4 v123, v114, 1.0 op_sel:[1,0,0]
	v_cvt_scalef32_pk_f16_fp4 v124, v114, 1.0 op_sel:[0,1,0]
	v_cvt_scalef32_pk_f16_fp4 v125, v114, 1.0 op_sel:[1,1,0]
	v_cvt_scalef32_pk_f16_fp4 v126, v116, 1.0
	v_cvt_scalef32_pk_f16_fp4 v127, v116, 1.0 op_sel:[1,0,0]
	v_cvt_scalef32_pk_f16_fp4 v128, v116, 1.0 op_sel:[0,1,0]
	v_cvt_scalef32_pk_f16_fp4 v129, v116, 1.0 op_sel:[1,1,0]
	v_mfma_f32_16x16x32_f16 v[50:53], v[66:69], v[122:125], 0
	v_cvt_scalef32_pk_f16_fp4 v122, v117, 1.0
	v_cvt_scalef32_pk_f16_fp4 v123, v117, 1.0 op_sel:[1,0,0]
	v_cvt_scalef32_pk_f16_fp4 v124, v117, 1.0 op_sel:[0,1,0]
	v_cvt_scalef32_pk_f16_fp4 v125, v117, 1.0 op_sel:[1,1,0]
	v_mfma_f32_16x16x32_f16 v[54:57], v[66:69], v[126:129], 0
	v_cvt_scalef32_pk_f16_fp4 v126, v115, 1.0
	v_cvt_scalef32_pk_f16_fp4 v127, v115, 1.0 op_sel:[1,0,0]
	v_cvt_scalef32_pk_f16_fp4 v128, v115, 1.0 op_sel:[0,1,0]
	v_cvt_scalef32_pk_f16_fp4 v129, v115, 1.0 op_sel:[1,1,0]
	v_mfma_f32_16x16x32_f16 v[50:53], v[74:77], v[122:125], v[50:53]
	v_mfma_f32_16x16x32_f16 v[54:57], v[74:77], v[126:129], v[54:57]
	s_waitcnt vmcnt(10)
	ds_read_b64_tr_b4 v[114:115], v150 offset:8192
	ds_read_b64_tr_b4 v[116:117], v158 offset:8192
	s_waitcnt lgkmcnt(2)
	s_add_i32 m0, s38, 0x0
	v_mad_u32_u16 v178, v106, v198, v166
	global_load_lds_dwordx4 v178, s[40:41]
	s_add_i32 m0, s38, 0x400
	v_mad_u32_u16 v179, v106, v198, v167 op_sel:[1,0,0,0]
	global_load_lds_dwordx4 v179, s[40:41]
	s_add_i32 m0, s38, 0x800
	v_mad_u32_u16 v178, v107, v198, v168
	global_load_lds_dwordx4 v178, s[40:41]
	s_add_i32 m0, s38, 0xc00
	v_mad_u32_u16 v179, v107, v198, v169 op_sel:[1,0,0,0]
	global_load_lds_dwordx4 v179, s[40:41]
	s_add_i32 m0, s38, 0x1000
	v_mad_u32_u16 v178, v108, v198, v170
	global_load_lds_dwordx4 v178, s[40:41]
	s_add_i32 m0, s38, 0x1400
	v_mad_u32_u16 v179, v108, v198, v171 op_sel:[1,0,0,0]
	global_load_lds_dwordx4 v179, s[40:41]
	s_add_i32 m0, s38, 0x1800
	v_mad_u32_u16 v178, v109, v198, v172
	global_load_lds_dwordx4 v178, s[40:41]
	s_add_i32 m0, s38, 0x1c00
	v_mad_u32_u16 v179, v109, v198, v173 op_sel:[1,0,0,0]
	global_load_lds_dwordx4 v179, s[40:41]
	v_cvt_scalef32_pk_f16_fp4 v122, v118, 1.0
	v_cvt_scalef32_pk_f16_fp4 v123, v118, 1.0 op_sel:[1,0,0]
	v_cvt_scalef32_pk_f16_fp4 v124, v118, 1.0 op_sel:[0,1,0]
	v_cvt_scalef32_pk_f16_fp4 v125, v118, 1.0 op_sel:[1,1,0]
	v_cvt_scalef32_pk_f16_fp4 v126, v120, 1.0
	v_cvt_scalef32_pk_f16_fp4 v127, v120, 1.0 op_sel:[1,0,0]
	v_cvt_scalef32_pk_f16_fp4 v128, v120, 1.0 op_sel:[0,1,0]
	v_cvt_scalef32_pk_f16_fp4 v129, v120, 1.0 op_sel:[1,1,0]
	v_mfma_f32_16x16x32_f16 v[58:61], v[66:69], v[122:125], 0
	v_cvt_scalef32_pk_f16_fp4 v122, v121, 1.0
	v_cvt_scalef32_pk_f16_fp4 v123, v121, 1.0 op_sel:[1,0,0]
	v_cvt_scalef32_pk_f16_fp4 v124, v121, 1.0 op_sel:[0,1,0]
	v_cvt_scalef32_pk_f16_fp4 v125, v121, 1.0 op_sel:[1,1,0]
	v_mfma_f32_16x16x32_f16 v[62:65], v[66:69], v[126:129], 0
	v_cvt_scalef32_pk_f16_fp4 v126, v119, 1.0
	v_cvt_scalef32_pk_f16_fp4 v127, v119, 1.0 op_sel:[1,0,0]
	v_cvt_scalef32_pk_f16_fp4 v128, v119, 1.0 op_sel:[0,1,0]
	v_cvt_scalef32_pk_f16_fp4 v129, v119, 1.0 op_sel:[1,1,0]
	v_mfma_f32_16x16x32_f16 v[58:61], v[74:77], v[122:125], v[58:61]
	v_mfma_f32_16x16x32_f16 v[62:65], v[74:77], v[126:129], v[62:65]
	ds_read_b64_tr_b4 v[118:119], v151 offset:8192
	ds_read_b64_tr_b4 v[120:121], v159 offset:8192
	s_waitcnt lgkmcnt(2)
	v_cvt_scalef32_pk_f16_fp4 v122, v114, 1.0
	v_cvt_scalef32_pk_f16_fp4 v123, v114, 1.0 op_sel:[1,0,0]
	v_cvt_scalef32_pk_f16_fp4 v124, v114, 1.0 op_sel:[0,1,0]
	v_cvt_scalef32_pk_f16_fp4 v125, v114, 1.0 op_sel:[1,1,0]
	v_cvt_scalef32_pk_f16_fp4 v126, v116, 1.0
	v_cvt_scalef32_pk_f16_fp4 v127, v116, 1.0 op_sel:[1,0,0]
	v_cvt_scalef32_pk_f16_fp4 v128, v116, 1.0 op_sel:[0,1,0]
	v_cvt_scalef32_pk_f16_fp4 v129, v116, 1.0 op_sel:[1,1,0]
	v_mfma_f32_16x16x32_f16 v[2:5], v[70:73], v[122:125], v[2:5]
	v_cvt_scalef32_pk_f16_fp4 v122, v117, 1.0
	v_cvt_scalef32_pk_f16_fp4 v123, v117, 1.0 op_sel:[1,0,0]
	v_cvt_scalef32_pk_f16_fp4 v124, v117, 1.0 op_sel:[0,1,0]
	v_cvt_scalef32_pk_f16_fp4 v125, v117, 1.0 op_sel:[1,1,0]
	v_mfma_f32_16x16x32_f16 v[6:9], v[70:73], v[126:129], v[6:9]
	v_cvt_scalef32_pk_f16_fp4 v126, v115, 1.0
	v_cvt_scalef32_pk_f16_fp4 v127, v115, 1.0 op_sel:[1,0,0]
	v_cvt_scalef32_pk_f16_fp4 v128, v115, 1.0 op_sel:[0,1,0]
	v_cvt_scalef32_pk_f16_fp4 v129, v115, 1.0 op_sel:[1,1,0]
	v_mfma_f32_16x16x32_f16 v[2:5], v[78:81], v[122:125], v[2:5]
	v_mfma_f32_16x16x32_f16 v[6:9], v[78:81], v[126:129], v[6:9]
	ds_read_b64_tr_b4 v[114:115], v152 offset:8192
	ds_read_b64_tr_b4 v[116:117], v160 offset:8192
	s_waitcnt lgkmcnt(2)
	v_cvt_scalef32_pk_f16_fp4 v122, v118, 1.0
	v_cvt_scalef32_pk_f16_fp4 v123, v118, 1.0 op_sel:[1,0,0]
	v_cvt_scalef32_pk_f16_fp4 v124, v118, 1.0 op_sel:[0,1,0]
	v_cvt_scalef32_pk_f16_fp4 v125, v118, 1.0 op_sel:[1,1,0]
	v_cvt_scalef32_pk_f16_fp4 v126, v120, 1.0
	v_cvt_scalef32_pk_f16_fp4 v127, v120, 1.0 op_sel:[1,0,0]
	v_cvt_scalef32_pk_f16_fp4 v128, v120, 1.0 op_sel:[0,1,0]
	v_cvt_scalef32_pk_f16_fp4 v129, v120, 1.0 op_sel:[1,1,0]
	v_mfma_f32_16x16x32_f16 v[10:13], v[70:73], v[122:125], v[10:13]
	v_cvt_scalef32_pk_f16_fp4 v122, v121, 1.0
	v_cvt_scalef32_pk_f16_fp4 v123, v121, 1.0 op_sel:[1,0,0]
	v_cvt_scalef32_pk_f16_fp4 v124, v121, 1.0 op_sel:[0,1,0]
	v_cvt_scalef32_pk_f16_fp4 v125, v121, 1.0 op_sel:[1,1,0]
	v_mfma_f32_16x16x32_f16 v[14:17], v[70:73], v[126:129], v[14:17]
	v_cvt_scalef32_pk_f16_fp4 v126, v119, 1.0
	v_cvt_scalef32_pk_f16_fp4 v127, v119, 1.0 op_sel:[1,0,0]
	v_cvt_scalef32_pk_f16_fp4 v128, v119, 1.0 op_sel:[0,1,0]
	v_cvt_scalef32_pk_f16_fp4 v129, v119, 1.0 op_sel:[1,1,0]
	v_mfma_f32_16x16x32_f16 v[10:13], v[78:81], v[122:125], v[10:13]
	v_mfma_f32_16x16x32_f16 v[14:17], v[78:81], v[126:129], v[14:17]
	ds_read_b64_tr_b4 v[118:119], v153 offset:8192
	ds_read_b64_tr_b4 v[120:121], v161 offset:8192
	s_waitcnt lgkmcnt(2)
	v_cvt_scalef32_pk_f16_fp4 v122, v114, 1.0
	v_cvt_scalef32_pk_f16_fp4 v123, v114, 1.0 op_sel:[1,0,0]
	v_cvt_scalef32_pk_f16_fp4 v124, v114, 1.0 op_sel:[0,1,0]
	v_cvt_scalef32_pk_f16_fp4 v125, v114, 1.0 op_sel:[1,1,0]
	v_cvt_scalef32_pk_f16_fp4 v126, v116, 1.0
	v_cvt_scalef32_pk_f16_fp4 v127, v116, 1.0 op_sel:[1,0,0]
	v_cvt_scalef32_pk_f16_fp4 v128, v116, 1.0 op_sel:[0,1,0]
	v_cvt_scalef32_pk_f16_fp4 v129, v116, 1.0 op_sel:[1,1,0]
	v_mfma_f32_16x16x32_f16 v[18:21], v[70:73], v[122:125], v[18:21]
	v_cvt_scalef32_pk_f16_fp4 v122, v117, 1.0
	v_cvt_scalef32_pk_f16_fp4 v123, v117, 1.0 op_sel:[1,0,0]
	v_cvt_scalef32_pk_f16_fp4 v124, v117, 1.0 op_sel:[0,1,0]
	v_cvt_scalef32_pk_f16_fp4 v125, v117, 1.0 op_sel:[1,1,0]
	v_mfma_f32_16x16x32_f16 v[22:25], v[70:73], v[126:129], v[22:25]
	v_cvt_scalef32_pk_f16_fp4 v126, v115, 1.0
	v_cvt_scalef32_pk_f16_fp4 v127, v115, 1.0 op_sel:[1,0,0]
	v_cvt_scalef32_pk_f16_fp4 v128, v115, 1.0 op_sel:[0,1,0]
	v_cvt_scalef32_pk_f16_fp4 v129, v115, 1.0 op_sel:[1,1,0]
	v_mfma_f32_16x16x32_f16 v[18:21], v[78:81], v[122:125], v[18:21]
	v_mfma_f32_16x16x32_f16 v[22:25], v[78:81], v[126:129], v[22:25]
	ds_read_b64_tr_b4 v[114:115], v154 offset:8192
	ds_read_b64_tr_b4 v[116:117], v162 offset:8192
	s_waitcnt lgkmcnt(2)
	v_cvt_scalef32_pk_f16_fp4 v122, v118, 1.0
	v_cvt_scalef32_pk_f16_fp4 v123, v118, 1.0 op_sel:[1,0,0]
	v_cvt_scalef32_pk_f16_fp4 v124, v118, 1.0 op_sel:[0,1,0]
	v_cvt_scalef32_pk_f16_fp4 v125, v118, 1.0 op_sel:[1,1,0]
	v_cvt_scalef32_pk_f16_fp4 v126, v120, 1.0
	v_cvt_scalef32_pk_f16_fp4 v127, v120, 1.0 op_sel:[1,0,0]
	v_cvt_scalef32_pk_f16_fp4 v128, v120, 1.0 op_sel:[0,1,0]
	v_cvt_scalef32_pk_f16_fp4 v129, v120, 1.0 op_sel:[1,1,0]
	v_mfma_f32_16x16x32_f16 v[26:29], v[70:73], v[122:125], v[26:29]
	v_cvt_scalef32_pk_f16_fp4 v122, v121, 1.0
	v_cvt_scalef32_pk_f16_fp4 v123, v121, 1.0 op_sel:[1,0,0]
	v_cvt_scalef32_pk_f16_fp4 v124, v121, 1.0 op_sel:[0,1,0]
	v_cvt_scalef32_pk_f16_fp4 v125, v121, 1.0 op_sel:[1,1,0]
	v_mfma_f32_16x16x32_f16 v[30:33], v[70:73], v[126:129], v[30:33]
	v_cvt_scalef32_pk_f16_fp4 v126, v119, 1.0
	v_cvt_scalef32_pk_f16_fp4 v127, v119, 1.0 op_sel:[1,0,0]
	v_cvt_scalef32_pk_f16_fp4 v128, v119, 1.0 op_sel:[0,1,0]
	v_cvt_scalef32_pk_f16_fp4 v129, v119, 1.0 op_sel:[1,1,0]
	v_mfma_f32_16x16x32_f16 v[26:29], v[78:81], v[122:125], v[26:29]
	v_mfma_f32_16x16x32_f16 v[30:33], v[78:81], v[126:129], v[30:33]
	ds_read_b64_tr_b4 v[118:119], v155 offset:8192
	ds_read_b64_tr_b4 v[120:121], v163 offset:8192
	s_waitcnt lgkmcnt(2)
	v_cvt_scalef32_pk_f16_fp4 v122, v114, 1.0
	v_cvt_scalef32_pk_f16_fp4 v123, v114, 1.0 op_sel:[1,0,0]
	v_cvt_scalef32_pk_f16_fp4 v124, v114, 1.0 op_sel:[0,1,0]
	v_cvt_scalef32_pk_f16_fp4 v125, v114, 1.0 op_sel:[1,1,0]
	v_cvt_scalef32_pk_f16_fp4 v126, v116, 1.0
	v_cvt_scalef32_pk_f16_fp4 v127, v116, 1.0 op_sel:[1,0,0]
	v_cvt_scalef32_pk_f16_fp4 v128, v116, 1.0 op_sel:[0,1,0]
	v_cvt_scalef32_pk_f16_fp4 v129, v116, 1.0 op_sel:[1,1,0]
	v_mfma_f32_16x16x32_f16 v[34:37], v[70:73], v[122:125], v[34:37]
	v_cvt_scalef32_pk_f16_fp4 v122, v117, 1.0
	v_cvt_scalef32_pk_f16_fp4 v123, v117, 1.0 op_sel:[1,0,0]
	v_cvt_scalef32_pk_f16_fp4 v124, v117, 1.0 op_sel:[0,1,0]
	v_cvt_scalef32_pk_f16_fp4 v125, v117, 1.0 op_sel:[1,1,0]
	v_mfma_f32_16x16x32_f16 v[38:41], v[70:73], v[126:129], v[38:41]
	v_cvt_scalef32_pk_f16_fp4 v126, v115, 1.0
	v_cvt_scalef32_pk_f16_fp4 v127, v115, 1.0 op_sel:[1,0,0]
	v_cvt_scalef32_pk_f16_fp4 v128, v115, 1.0 op_sel:[0,1,0]
	v_cvt_scalef32_pk_f16_fp4 v129, v115, 1.0 op_sel:[1,1,0]
	v_mfma_f32_16x16x32_f16 v[34:37], v[78:81], v[122:125], v[34:37]
	v_mfma_f32_16x16x32_f16 v[38:41], v[78:81], v[126:129], v[38:41]
	ds_read_b64_tr_b4 v[114:115], v156 offset:8192
	ds_read_b64_tr_b4 v[116:117], v164 offset:8192
	s_waitcnt lgkmcnt(2)
	v_cvt_scalef32_pk_f16_fp4 v122, v118, 1.0
	v_cvt_scalef32_pk_f16_fp4 v123, v118, 1.0 op_sel:[1,0,0]
	v_cvt_scalef32_pk_f16_fp4 v124, v118, 1.0 op_sel:[0,1,0]
	v_cvt_scalef32_pk_f16_fp4 v125, v118, 1.0 op_sel:[1,1,0]
	v_cvt_scalef32_pk_f16_fp4 v126, v120, 1.0
	v_cvt_scalef32_pk_f16_fp4 v127, v120, 1.0 op_sel:[1,0,0]
	v_cvt_scalef32_pk_f16_fp4 v128, v120, 1.0 op_sel:[0,1,0]
	v_cvt_scalef32_pk_f16_fp4 v129, v120, 1.0 op_sel:[1,1,0]
	v_mfma_f32_16x16x32_f16 v[42:45], v[70:73], v[122:125], v[42:45]
	v_cvt_scalef32_pk_f16_fp4 v122, v121, 1.0
	v_cvt_scalef32_pk_f16_fp4 v123, v121, 1.0 op_sel:[1,0,0]
	v_cvt_scalef32_pk_f16_fp4 v124, v121, 1.0 op_sel:[0,1,0]
	v_cvt_scalef32_pk_f16_fp4 v125, v121, 1.0 op_sel:[1,1,0]
	v_mfma_f32_16x16x32_f16 v[46:49], v[70:73], v[126:129], v[46:49]
	v_cvt_scalef32_pk_f16_fp4 v126, v119, 1.0
	v_cvt_scalef32_pk_f16_fp4 v127, v119, 1.0 op_sel:[1,0,0]
	v_cvt_scalef32_pk_f16_fp4 v128, v119, 1.0 op_sel:[0,1,0]
	v_cvt_scalef32_pk_f16_fp4 v129, v119, 1.0 op_sel:[1,1,0]
	v_mfma_f32_16x16x32_f16 v[42:45], v[78:81], v[122:125], v[42:45]
	v_mfma_f32_16x16x32_f16 v[46:49], v[78:81], v[126:129], v[46:49]
	ds_read_b64_tr_b4 v[118:119], v157 offset:8192
	ds_read_b64_tr_b4 v[120:121], v165 offset:8192
	s_waitcnt lgkmcnt(2)
	v_cvt_scalef32_pk_f16_fp4 v122, v114, 1.0
	v_cvt_scalef32_pk_f16_fp4 v123, v114, 1.0 op_sel:[1,0,0]
	v_cvt_scalef32_pk_f16_fp4 v124, v114, 1.0 op_sel:[0,1,0]
	v_cvt_scalef32_pk_f16_fp4 v125, v114, 1.0 op_sel:[1,1,0]
	v_cvt_scalef32_pk_f16_fp4 v126, v116, 1.0
	v_cvt_scalef32_pk_f16_fp4 v127, v116, 1.0 op_sel:[1,0,0]
	v_cvt_scalef32_pk_f16_fp4 v128, v116, 1.0 op_sel:[0,1,0]
	v_cvt_scalef32_pk_f16_fp4 v129, v116, 1.0 op_sel:[1,1,0]
	v_mfma_f32_16x16x32_f16 v[50:53], v[70:73], v[122:125], v[50:53]
	v_cvt_scalef32_pk_f16_fp4 v122, v117, 1.0
	v_cvt_scalef32_pk_f16_fp4 v123, v117, 1.0 op_sel:[1,0,0]
	v_cvt_scalef32_pk_f16_fp4 v124, v117, 1.0 op_sel:[0,1,0]
	v_cvt_scalef32_pk_f16_fp4 v125, v117, 1.0 op_sel:[1,1,0]
	v_mfma_f32_16x16x32_f16 v[54:57], v[70:73], v[126:129], v[54:57]
	v_cvt_scalef32_pk_f16_fp4 v126, v115, 1.0
	v_cvt_scalef32_pk_f16_fp4 v127, v115, 1.0 op_sel:[1,0,0]
	v_cvt_scalef32_pk_f16_fp4 v128, v115, 1.0 op_sel:[0,1,0]
	v_cvt_scalef32_pk_f16_fp4 v129, v115, 1.0 op_sel:[1,1,0]
	v_mfma_f32_16x16x32_f16 v[50:53], v[78:81], v[122:125], v[50:53]
	v_mfma_f32_16x16x32_f16 v[54:57], v[78:81], v[126:129], v[54:57]
	s_waitcnt vmcnt(0)
	ds_read_b64_tr_b4 v[114:115], v150
	ds_read_b64_tr_b4 v[116:117], v158
	s_waitcnt lgkmcnt(2)
	s_add_i32 m0, s38, 0x2000
	v_mad_u32_u16 v178, v110, v198, v166
	global_load_lds_dwordx4 v178, s[40:41]
	s_add_i32 m0, s38, 0x2400
	v_mad_u32_u16 v179, v110, v198, v167 op_sel:[1,0,0,0]
	global_load_lds_dwordx4 v179, s[40:41]
	s_add_i32 m0, s38, 0x2800
	v_mad_u32_u16 v178, v111, v198, v168
	global_load_lds_dwordx4 v178, s[40:41]
	s_add_i32 m0, s38, 0x2c00
	v_mad_u32_u16 v179, v111, v198, v169 op_sel:[1,0,0,0]
	global_load_lds_dwordx4 v179, s[40:41]
	s_add_i32 m0, s38, 0x3000
	v_mad_u32_u16 v178, v112, v198, v170
	global_load_lds_dwordx4 v178, s[40:41]
	s_add_i32 m0, s38, 0x3400
	v_mad_u32_u16 v179, v112, v198, v171 op_sel:[1,0,0,0]
	global_load_lds_dwordx4 v179, s[40:41]
	s_add_i32 m0, s38, 0x3800
	v_mad_u32_u16 v178, v113, v198, v172
	global_load_lds_dwordx4 v178, s[40:41]
	s_add_i32 m0, s38, 0x3c00
	v_mad_u32_u16 v179, v113, v198, v173 op_sel:[1,0,0,0]
	global_load_lds_dwordx4 v179, s[40:41]
	ds_read_b128 v[82:85], v174 offset:256
	ds_read_b128 v[86:89], v174 offset:272
	ds_read_b128 v[90:93], v175 offset:256
	ds_read_b128 v[94:97], v175 offset:272
	ds_read_b128 v[98:101], v199
	ds_read_b128 v[102:105], v199 offset:16
	v_cvt_scalef32_pk_f16_fp4 v122, v118, 1.0
	v_cvt_scalef32_pk_f16_fp4 v123, v118, 1.0 op_sel:[1,0,0]
	v_cvt_scalef32_pk_f16_fp4 v124, v118, 1.0 op_sel:[0,1,0]
	v_cvt_scalef32_pk_f16_fp4 v125, v118, 1.0 op_sel:[1,1,0]
	v_cvt_scalef32_pk_f16_fp4 v126, v120, 1.0
	v_cvt_scalef32_pk_f16_fp4 v127, v120, 1.0 op_sel:[1,0,0]
	v_cvt_scalef32_pk_f16_fp4 v128, v120, 1.0 op_sel:[0,1,0]
	v_cvt_scalef32_pk_f16_fp4 v129, v120, 1.0 op_sel:[1,1,0]
	v_mfma_f32_16x16x32_f16 v[58:61], v[70:73], v[122:125], v[58:61]
	v_cvt_scalef32_pk_f16_fp4 v122, v121, 1.0
	v_cvt_scalef32_pk_f16_fp4 v123, v121, 1.0 op_sel:[1,0,0]
	v_cvt_scalef32_pk_f16_fp4 v124, v121, 1.0 op_sel:[0,1,0]
	v_cvt_scalef32_pk_f16_fp4 v125, v121, 1.0 op_sel:[1,1,0]
	v_mfma_f32_16x16x32_f16 v[62:65], v[70:73], v[126:129], v[62:65]
	v_cvt_scalef32_pk_f16_fp4 v126, v119, 1.0
	v_cvt_scalef32_pk_f16_fp4 v127, v119, 1.0 op_sel:[1,0,0]
	v_cvt_scalef32_pk_f16_fp4 v128, v119, 1.0 op_sel:[0,1,0]
	v_cvt_scalef32_pk_f16_fp4 v129, v119, 1.0 op_sel:[1,1,0]
	v_mfma_f32_16x16x32_f16 v[58:61], v[78:81], v[122:125], v[58:61]
	v_mfma_f32_16x16x32_f16 v[62:65], v[78:81], v[126:129], v[62:65]
	s_nop 7
	v_cmp_ne_u32_e32 vcc, 0, v196
	v_cndmask_b32_e32 v146, v2, v6, vcc
	v_cndmask_b32_e32 v142, v10, v14, vcc
	v_cndmask_b32_e32 v147, v18, v22, vcc
	v_cndmask_b32_e32 v143, v26, v30, vcc
	v_cndmask_b32_e32 v148, v34, v38, vcc
	v_cndmask_b32_e32 v144, v42, v46, vcc
	v_cndmask_b32_e32 v149, v50, v54, vcc
	v_cndmask_b32_e32 v145, v58, v62, vcc
	v_cmp_ne_u32_e32 vcc, 0, v197
	v_cndmask_b32_e32 v146, v146, v142, vcc
	v_cndmask_b32_e32 v147, v147, v143, vcc
	v_cndmask_b32_e32 v148, v148, v144, vcc
	v_cndmask_b32_e32 v149, v149, v145, vcc
	v_fma_f32 v142, v134, v146, v130
	v_fma_f32 v143, v135, v147, v131
	v_fma_f32 v144, v136, v148, v132
	v_fma_f32 v145, v137, v149, v133
	global_store_dword v[180:181], v142, off
	global_store_dword v[180:181], v143, off offset:256
	global_store_dword v[180:181], v144, off offset:512
	global_store_dword v[180:181], v145, off offset:768
	v_lshl_add_u64 v[180:181], v[180:181], 0, s[48:49]
	s_lshr_b32 s99, s38, 4
	s_add_i32 m0, s99, 0x21000
	s_mov_b64 exec, 0xffff
	global_load_lds_dwordx4 v177, s[0:1]
	s_mov_b64 exec, -1
	v_add_u32_e32 v177, 0x100, v177
	s_lshr_b32 s99, s38, 5
	s_add_i32 m0, s99, 0x23100
	s_mov_b64 exec, 0xffff
	global_load_lds_dwordx4 v176, s[22:23]
	s_mov_b64 exec, -1
	s_lshl_b32 s99, s43, 8
	s_cmp_eq_u32 s33, 4
	s_cselect_b32 s99, s99, 0x100
	v_add_u32_e32 v176, s99, v176
	global_load_dword v130, v[180:181], off
	global_load_dword v131, v[180:181], off offset:256
	global_load_dword v132, v[180:181], off offset:512
	global_load_dword v133, v[180:181], off offset:768
	ds_read_b64_tr_b4 v[118:119], v151
	ds_read_b64_tr_b4 v[120:121], v159
	s_waitcnt lgkmcnt(2)
	v_cvt_scalef32_pk_f16_fp4 v122, v114, 1.0
	v_cvt_scalef32_pk_f16_fp4 v123, v114, 1.0 op_sel:[1,0,0]
	v_cvt_scalef32_pk_f16_fp4 v124, v114, 1.0 op_sel:[0,1,0]
	v_cvt_scalef32_pk_f16_fp4 v125, v114, 1.0 op_sel:[1,1,0]
	v_cvt_scalef32_pk_f16_fp4 v126, v116, 1.0
	v_cvt_scalef32_pk_f16_fp4 v127, v116, 1.0 op_sel:[1,0,0]
	v_cvt_scalef32_pk_f16_fp4 v128, v116, 1.0 op_sel:[0,1,0]
	v_cvt_scalef32_pk_f16_fp4 v129, v116, 1.0 op_sel:[1,1,0]
	v_mfma_f32_16x16x32_f16 v[2:5], v[82:85], v[122:125], 0
	v_cvt_scalef32_pk_f16_fp4 v122, v117, 1.0
	v_cvt_scalef32_pk_f16_fp4 v123, v117, 1.0 op_sel:[1,0,0]
	v_cvt_scalef32_pk_f16_fp4 v124, v117, 1.0 op_sel:[0,1,0]
	v_cvt_scalef32_pk_f16_fp4 v125, v117, 1.0 op_sel:[1,1,0]
	v_mfma_f32_16x16x32_f16 v[6:9], v[82:85], v[126:129], 0
	v_cvt_scalef32_pk_f16_fp4 v126, v115, 1.0
	v_cvt_scalef32_pk_f16_fp4 v127, v115, 1.0 op_sel:[1,0,0]
	v_cvt_scalef32_pk_f16_fp4 v128, v115, 1.0 op_sel:[0,1,0]
	v_cvt_scalef32_pk_f16_fp4 v129, v115, 1.0 op_sel:[1,1,0]
	v_mfma_f32_16x16x32_f16 v[2:5], v[90:93], v[122:125], v[2:5]
	v_mfma_f32_16x16x32_f16 v[6:9], v[90:93], v[126:129], v[6:9]
	ds_read_b64_tr_b4 v[114:115], v152
	ds_read_b64_tr_b4 v[116:117], v160
	s_waitcnt lgkmcnt(2)
	v_cvt_scalef32_pk_f16_fp4 v122, v118, 1.0
	v_cvt_scalef32_pk_f16_fp4 v123, v118, 1.0 op_sel:[1,0,0]
	v_cvt_scalef32_pk_f16_fp4 v124, v118, 1.0 op_sel:[0,1,0]
	v_cvt_scalef32_pk_f16_fp4 v125, v118, 1.0 op_sel:[1,1,0]
	v_cvt_scalef32_pk_f16_fp4 v126, v120, 1.0
	v_cvt_scalef32_pk_f16_fp4 v127, v120, 1.0 op_sel:[1,0,0]
	v_cvt_scalef32_pk_f16_fp4 v128, v120, 1.0 op_sel:[0,1,0]
	v_cvt_scalef32_pk_f16_fp4 v129, v120, 1.0 op_sel:[1,1,0]
	v_mfma_f32_16x16x32_f16 v[10:13], v[82:85], v[122:125], 0
	v_cvt_scalef32_pk_f16_fp4 v122, v121, 1.0
	v_cvt_scalef32_pk_f16_fp4 v123, v121, 1.0 op_sel:[1,0,0]
	v_cvt_scalef32_pk_f16_fp4 v124, v121, 1.0 op_sel:[0,1,0]
	v_cvt_scalef32_pk_f16_fp4 v125, v121, 1.0 op_sel:[1,1,0]
	v_mfma_f32_16x16x32_f16 v[14:17], v[82:85], v[126:129], 0
	v_cvt_scalef32_pk_f16_fp4 v126, v119, 1.0
	v_cvt_scalef32_pk_f16_fp4 v127, v119, 1.0 op_sel:[1,0,0]
	v_cvt_scalef32_pk_f16_fp4 v128, v119, 1.0 op_sel:[0,1,0]
	v_cvt_scalef32_pk_f16_fp4 v129, v119, 1.0 op_sel:[1,1,0]
	v_mfma_f32_16x16x32_f16 v[10:13], v[90:93], v[122:125], v[10:13]
	v_mfma_f32_16x16x32_f16 v[14:17], v[90:93], v[126:129], v[14:17]
	ds_read_b64_tr_b4 v[118:119], v153
	ds_read_b64_tr_b4 v[120:121], v161
	s_waitcnt lgkmcnt(2)
	v_cvt_scalef32_pk_f16_fp4 v122, v114, 1.0
	v_cvt_scalef32_pk_f16_fp4 v123, v114, 1.0 op_sel:[1,0,0]
	v_cvt_scalef32_pk_f16_fp4 v124, v114, 1.0 op_sel:[0,1,0]
	v_cvt_scalef32_pk_f16_fp4 v125, v114, 1.0 op_sel:[1,1,0]
	v_cvt_scalef32_pk_f16_fp4 v126, v116, 1.0
	v_cvt_scalef32_pk_f16_fp4 v127, v116, 1.0 op_sel:[1,0,0]
	v_cvt_scalef32_pk_f16_fp4 v128, v116, 1.0 op_sel:[0,1,0]
	v_cvt_scalef32_pk_f16_fp4 v129, v116, 1.0 op_sel:[1,1,0]
	v_mfma_f32_16x16x32_f16 v[18:21], v[82:85], v[122:125], 0
	v_cvt_scalef32_pk_f16_fp4 v122, v117, 1.0
	v_cvt_scalef32_pk_f16_fp4 v123, v117, 1.0 op_sel:[1,0,0]
	v_cvt_scalef32_pk_f16_fp4 v124, v117, 1.0 op_sel:[0,1,0]
	v_cvt_scalef32_pk_f16_fp4 v125, v117, 1.0 op_sel:[1,1,0]
	v_mfma_f32_16x16x32_f16 v[22:25], v[82:85], v[126:129], 0
	v_cvt_scalef32_pk_f16_fp4 v126, v115, 1.0
	v_cvt_scalef32_pk_f16_fp4 v127, v115, 1.0 op_sel:[1,0,0]
	v_cvt_scalef32_pk_f16_fp4 v128, v115, 1.0 op_sel:[0,1,0]
	v_cvt_scalef32_pk_f16_fp4 v129, v115, 1.0 op_sel:[1,1,0]
	v_mfma_f32_16x16x32_f16 v[18:21], v[90:93], v[122:125], v[18:21]
	v_mfma_f32_16x16x32_f16 v[22:25], v[90:93], v[126:129], v[22:25]
	ds_read_b64_tr_b4 v[114:115], v154
	ds_read_b64_tr_b4 v[116:117], v162
	s_waitcnt lgkmcnt(2)
	v_cvt_scalef32_pk_f16_fp4 v122, v118, 1.0
	v_cvt_scalef32_pk_f16_fp4 v123, v118, 1.0 op_sel:[1,0,0]
	v_cvt_scalef32_pk_f16_fp4 v124, v118, 1.0 op_sel:[0,1,0]
	v_cvt_scalef32_pk_f16_fp4 v125, v118, 1.0 op_sel:[1,1,0]
	v_cvt_scalef32_pk_f16_fp4 v126, v120, 1.0
	v_cvt_scalef32_pk_f16_fp4 v127, v120, 1.0 op_sel:[1,0,0]
	v_cvt_scalef32_pk_f16_fp4 v128, v120, 1.0 op_sel:[0,1,0]
	v_cvt_scalef32_pk_f16_fp4 v129, v120, 1.0 op_sel:[1,1,0]
	v_mfma_f32_16x16x32_f16 v[26:29], v[82:85], v[122:125], 0
	v_cvt_scalef32_pk_f16_fp4 v122, v121, 1.0
	v_cvt_scalef32_pk_f16_fp4 v123, v121, 1.0 op_sel:[1,0,0]
	v_cvt_scalef32_pk_f16_fp4 v124, v121, 1.0 op_sel:[0,1,0]
	v_cvt_scalef32_pk_f16_fp4 v125, v121, 1.0 op_sel:[1,1,0]
	v_mfma_f32_16x16x32_f16 v[30:33], v[82:85], v[126:129], 0
	v_cvt_scalef32_pk_f16_fp4 v126, v119, 1.0
	v_cvt_scalef32_pk_f16_fp4 v127, v119, 1.0 op_sel:[1,0,0]
	v_cvt_scalef32_pk_f16_fp4 v128, v119, 1.0 op_sel:[0,1,0]
	v_cvt_scalef32_pk_f16_fp4 v129, v119, 1.0 op_sel:[1,1,0]
	v_mfma_f32_16x16x32_f16 v[26:29], v[90:93], v[122:125], v[26:29]
	v_mfma_f32_16x16x32_f16 v[30:33], v[90:93], v[126:129], v[30:33]
	ds_read_b64_tr_b4 v[118:119], v155
	ds_read_b64_tr_b4 v[120:121], v163
	s_waitcnt lgkmcnt(2)
	v_cvt_scalef32_pk_f16_fp4 v122, v114, 1.0
	v_cvt_scalef32_pk_f16_fp4 v123, v114, 1.0 op_sel:[1,0,0]
	v_cvt_scalef32_pk_f16_fp4 v124, v114, 1.0 op_sel:[0,1,0]
	v_cvt_scalef32_pk_f16_fp4 v125, v114, 1.0 op_sel:[1,1,0]
	v_cvt_scalef32_pk_f16_fp4 v126, v116, 1.0
	v_cvt_scalef32_pk_f16_fp4 v127, v116, 1.0 op_sel:[1,0,0]
	v_cvt_scalef32_pk_f16_fp4 v128, v116, 1.0 op_sel:[0,1,0]
	v_cvt_scalef32_pk_f16_fp4 v129, v116, 1.0 op_sel:[1,1,0]
	v_mfma_f32_16x16x32_f16 v[34:37], v[82:85], v[122:125], 0
	v_cvt_scalef32_pk_f16_fp4 v122, v117, 1.0
	v_cvt_scalef32_pk_f16_fp4 v123, v117, 1.0 op_sel:[1,0,0]
	v_cvt_scalef32_pk_f16_fp4 v124, v117, 1.0 op_sel:[0,1,0]
	v_cvt_scalef32_pk_f16_fp4 v125, v117, 1.0 op_sel:[1,1,0]
	v_mfma_f32_16x16x32_f16 v[38:41], v[82:85], v[126:129], 0
	v_cvt_scalef32_pk_f16_fp4 v126, v115, 1.0
	v_cvt_scalef32_pk_f16_fp4 v127, v115, 1.0 op_sel:[1,0,0]
	v_cvt_scalef32_pk_f16_fp4 v128, v115, 1.0 op_sel:[0,1,0]
	v_cvt_scalef32_pk_f16_fp4 v129, v115, 1.0 op_sel:[1,1,0]
	v_mfma_f32_16x16x32_f16 v[34:37], v[90:93], v[122:125], v[34:37]
	v_mfma_f32_16x16x32_f16 v[38:41], v[90:93], v[126:129], v[38:41]
	ds_read_b64_tr_b4 v[114:115], v156
	ds_read_b64_tr_b4 v[116:117], v164
	s_waitcnt lgkmcnt(2)
	v_cvt_scalef32_pk_f16_fp4 v122, v118, 1.0
	v_cvt_scalef32_pk_f16_fp4 v123, v118, 1.0 op_sel:[1,0,0]
	v_cvt_scalef32_pk_f16_fp4 v124, v118, 1.0 op_sel:[0,1,0]
	v_cvt_scalef32_pk_f16_fp4 v125, v118, 1.0 op_sel:[1,1,0]
	v_cvt_scalef32_pk_f16_fp4 v126, v120, 1.0
	v_cvt_scalef32_pk_f16_fp4 v127, v120, 1.0 op_sel:[1,0,0]
	v_cvt_scalef32_pk_f16_fp4 v128, v120, 1.0 op_sel:[0,1,0]
	v_cvt_scalef32_pk_f16_fp4 v129, v120, 1.0 op_sel:[1,1,0]
	v_mfma_f32_16x16x32_f16 v[42:45], v[82:85], v[122:125], 0
	v_cvt_scalef32_pk_f16_fp4 v122, v121, 1.0
	v_cvt_scalef32_pk_f16_fp4 v123, v121, 1.0 op_sel:[1,0,0]
	v_cvt_scalef32_pk_f16_fp4 v124, v121, 1.0 op_sel:[0,1,0]
	v_cvt_scalef32_pk_f16_fp4 v125, v121, 1.0 op_sel:[1,1,0]
	v_mfma_f32_16x16x32_f16 v[46:49], v[82:85], v[126:129], 0
	v_cvt_scalef32_pk_f16_fp4 v126, v119, 1.0
	v_cvt_scalef32_pk_f16_fp4 v127, v119, 1.0 op_sel:[1,0,0]
	v_cvt_scalef32_pk_f16_fp4 v128, v119, 1.0 op_sel:[0,1,0]
	v_cvt_scalef32_pk_f16_fp4 v129, v119, 1.0 op_sel:[1,1,0]
	v_mfma_f32_16x16x32_f16 v[42:45], v[90:93], v[122:125], v[42:45]
	v_mfma_f32_16x16x32_f16 v[46:49], v[90:93], v[126:129], v[46:49]
	ds_read_b64_tr_b4 v[118:119], v157
	ds_read_b64_tr_b4 v[120:121], v165
	s_waitcnt lgkmcnt(2)
	v_cvt_scalef32_pk_f16_fp4 v122, v114, 1.0
	v_cvt_scalef32_pk_f16_fp4 v123, v114, 1.0 op_sel:[1,0,0]
	v_cvt_scalef32_pk_f16_fp4 v124, v114, 1.0 op_sel:[0,1,0]
	v_cvt_scalef32_pk_f16_fp4 v125, v114, 1.0 op_sel:[1,1,0]
	v_cvt_scalef32_pk_f16_fp4 v126, v116, 1.0
	v_cvt_scalef32_pk_f16_fp4 v127, v116, 1.0 op_sel:[1,0,0]
	v_cvt_scalef32_pk_f16_fp4 v128, v116, 1.0 op_sel:[0,1,0]
	v_cvt_scalef32_pk_f16_fp4 v129, v116, 1.0 op_sel:[1,1,0]
	v_mfma_f32_16x16x32_f16 v[50:53], v[82:85], v[122:125], 0
	v_cvt_scalef32_pk_f16_fp4 v122, v117, 1.0
	v_cvt_scalef32_pk_f16_fp4 v123, v117, 1.0 op_sel:[1,0,0]
	v_cvt_scalef32_pk_f16_fp4 v124, v117, 1.0 op_sel:[0,1,0]
	v_cvt_scalef32_pk_f16_fp4 v125, v117, 1.0 op_sel:[1,1,0]
	v_mfma_f32_16x16x32_f16 v[54:57], v[82:85], v[126:129], 0
	v_cvt_scalef32_pk_f16_fp4 v126, v115, 1.0
	v_cvt_scalef32_pk_f16_fp4 v127, v115, 1.0 op_sel:[1,0,0]
	v_cvt_scalef32_pk_f16_fp4 v128, v115, 1.0 op_sel:[0,1,0]
	v_cvt_scalef32_pk_f16_fp4 v129, v115, 1.0 op_sel:[1,1,0]
	v_mfma_f32_16x16x32_f16 v[50:53], v[90:93], v[122:125], v[50:53]
	v_mfma_f32_16x16x32_f16 v[54:57], v[90:93], v[126:129], v[54:57]
	s_waitcnt vmcnt(10)
	ds_read_b64_tr_b4 v[114:115], v150 offset:8192
	ds_read_b64_tr_b4 v[116:117], v158 offset:8192
	s_waitcnt lgkmcnt(2)
	s_add_i32 m0, s38, 0x0
	v_mad_u32_u16 v178, v98, v198, v166
	global_load_lds_dwordx4 v178, s[40:41]
	s_add_i32 m0, s38, 0x400
	v_mad_u32_u16 v179, v98, v198, v167 op_sel:[1,0,0,0]
	global_load_lds_dwordx4 v179, s[40:41]
	s_add_i32 m0, s38, 0x800
	v_mad_u32_u16 v178, v99, v198, v168
	global_load_lds_dwordx4 v178, s[40:41]
	s_add_i32 m0, s38, 0xc00
	v_mad_u32_u16 v179, v99, v198, v169 op_sel:[1,0,0,0]
	global_load_lds_dwordx4 v179, s[40:41]
	s_add_i32 m0, s38, 0x1000
	v_mad_u32_u16 v178, v100, v198, v170
	global_load_lds_dwordx4 v178, s[40:41]
	s_add_i32 m0, s38, 0x1400
	v_mad_u32_u16 v179, v100, v198, v171 op_sel:[1,0,0,0]
	global_load_lds_dwordx4 v179, s[40:41]
	s_add_i32 m0, s38, 0x1800
	v_mad_u32_u16 v178, v101, v198, v172
	global_load_lds_dwordx4 v178, s[40:41]
	s_add_i32 m0, s38, 0x1c00
	v_mad_u32_u16 v179, v101, v198, v173 op_sel:[1,0,0,0]
	global_load_lds_dwordx4 v179, s[40:41]
	v_cvt_scalef32_pk_f16_fp4 v122, v118, 1.0
	v_cvt_scalef32_pk_f16_fp4 v123, v118, 1.0 op_sel:[1,0,0]
	v_cvt_scalef32_pk_f16_fp4 v124, v118, 1.0 op_sel:[0,1,0]
	v_cvt_scalef32_pk_f16_fp4 v125, v118, 1.0 op_sel:[1,1,0]
	v_cvt_scalef32_pk_f16_fp4 v126, v120, 1.0
	v_cvt_scalef32_pk_f16_fp4 v127, v120, 1.0 op_sel:[1,0,0]
	v_cvt_scalef32_pk_f16_fp4 v128, v120, 1.0 op_sel:[0,1,0]
	v_cvt_scalef32_pk_f16_fp4 v129, v120, 1.0 op_sel:[1,1,0]
	v_mfma_f32_16x16x32_f16 v[58:61], v[82:85], v[122:125], 0
	v_cvt_scalef32_pk_f16_fp4 v122, v121, 1.0
	v_cvt_scalef32_pk_f16_fp4 v123, v121, 1.0 op_sel:[1,0,0]
	v_cvt_scalef32_pk_f16_fp4 v124, v121, 1.0 op_sel:[0,1,0]
	v_cvt_scalef32_pk_f16_fp4 v125, v121, 1.0 op_sel:[1,1,0]
	v_mfma_f32_16x16x32_f16 v[62:65], v[82:85], v[126:129], 0
	v_cvt_scalef32_pk_f16_fp4 v126, v119, 1.0
	v_cvt_scalef32_pk_f16_fp4 v127, v119, 1.0 op_sel:[1,0,0]
	v_cvt_scalef32_pk_f16_fp4 v128, v119, 1.0 op_sel:[0,1,0]
	v_cvt_scalef32_pk_f16_fp4 v129, v119, 1.0 op_sel:[1,1,0]
	v_mfma_f32_16x16x32_f16 v[58:61], v[90:93], v[122:125], v[58:61]
	v_mfma_f32_16x16x32_f16 v[62:65], v[90:93], v[126:129], v[62:65]
	ds_read_b64_tr_b4 v[118:119], v151 offset:8192
	ds_read_b64_tr_b4 v[120:121], v159 offset:8192
	s_waitcnt lgkmcnt(2)
	v_cvt_scalef32_pk_f16_fp4 v122, v114, 1.0
	v_cvt_scalef32_pk_f16_fp4 v123, v114, 1.0 op_sel:[1,0,0]
	v_cvt_scalef32_pk_f16_fp4 v124, v114, 1.0 op_sel:[0,1,0]
	v_cvt_scalef32_pk_f16_fp4 v125, v114, 1.0 op_sel:[1,1,0]
	v_cvt_scalef32_pk_f16_fp4 v126, v116, 1.0
	v_cvt_scalef32_pk_f16_fp4 v127, v116, 1.0 op_sel:[1,0,0]
	v_cvt_scalef32_pk_f16_fp4 v128, v116, 1.0 op_sel:[0,1,0]
	v_cvt_scalef32_pk_f16_fp4 v129, v116, 1.0 op_sel:[1,1,0]
	v_mfma_f32_16x16x32_f16 v[2:5], v[86:89], v[122:125], v[2:5]
	v_cvt_scalef32_pk_f16_fp4 v122, v117, 1.0
	v_cvt_scalef32_pk_f16_fp4 v123, v117, 1.0 op_sel:[1,0,0]
	v_cvt_scalef32_pk_f16_fp4 v124, v117, 1.0 op_sel:[0,1,0]
	v_cvt_scalef32_pk_f16_fp4 v125, v117, 1.0 op_sel:[1,1,0]
	v_mfma_f32_16x16x32_f16 v[6:9], v[86:89], v[126:129], v[6:9]
	v_cvt_scalef32_pk_f16_fp4 v126, v115, 1.0
	v_cvt_scalef32_pk_f16_fp4 v127, v115, 1.0 op_sel:[1,0,0]
	v_cvt_scalef32_pk_f16_fp4 v128, v115, 1.0 op_sel:[0,1,0]
	v_cvt_scalef32_pk_f16_fp4 v129, v115, 1.0 op_sel:[1,1,0]
	v_mfma_f32_16x16x32_f16 v[2:5], v[94:97], v[122:125], v[2:5]
	v_mfma_f32_16x16x32_f16 v[6:9], v[94:97], v[126:129], v[6:9]
	ds_read_b64_tr_b4 v[114:115], v152 offset:8192
	ds_read_b64_tr_b4 v[116:117], v160 offset:8192
	s_waitcnt lgkmcnt(2)
	v_cvt_scalef32_pk_f16_fp4 v122, v118, 1.0
	v_cvt_scalef32_pk_f16_fp4 v123, v118, 1.0 op_sel:[1,0,0]
	v_cvt_scalef32_pk_f16_fp4 v124, v118, 1.0 op_sel:[0,1,0]
	v_cvt_scalef32_pk_f16_fp4 v125, v118, 1.0 op_sel:[1,1,0]
	v_cvt_scalef32_pk_f16_fp4 v126, v120, 1.0
	v_cvt_scalef32_pk_f16_fp4 v127, v120, 1.0 op_sel:[1,0,0]
	v_cvt_scalef32_pk_f16_fp4 v128, v120, 1.0 op_sel:[0,1,0]
	v_cvt_scalef32_pk_f16_fp4 v129, v120, 1.0 op_sel:[1,1,0]
	v_mfma_f32_16x16x32_f16 v[10:13], v[86:89], v[122:125], v[10:13]
	v_cvt_scalef32_pk_f16_fp4 v122, v121, 1.0
	v_cvt_scalef32_pk_f16_fp4 v123, v121, 1.0 op_sel:[1,0,0]
	v_cvt_scalef32_pk_f16_fp4 v124, v121, 1.0 op_sel:[0,1,0]
	v_cvt_scalef32_pk_f16_fp4 v125, v121, 1.0 op_sel:[1,1,0]
	v_mfma_f32_16x16x32_f16 v[14:17], v[86:89], v[126:129], v[14:17]
	v_cvt_scalef32_pk_f16_fp4 v126, v119, 1.0
	v_cvt_scalef32_pk_f16_fp4 v127, v119, 1.0 op_sel:[1,0,0]
	v_cvt_scalef32_pk_f16_fp4 v128, v119, 1.0 op_sel:[0,1,0]
	v_cvt_scalef32_pk_f16_fp4 v129, v119, 1.0 op_sel:[1,1,0]
	v_mfma_f32_16x16x32_f16 v[10:13], v[94:97], v[122:125], v[10:13]
	v_mfma_f32_16x16x32_f16 v[14:17], v[94:97], v[126:129], v[14:17]
	ds_read_b64_tr_b4 v[118:119], v153 offset:8192
	ds_read_b64_tr_b4 v[120:121], v161 offset:8192
	s_waitcnt lgkmcnt(2)
	v_cvt_scalef32_pk_f16_fp4 v122, v114, 1.0
	v_cvt_scalef32_pk_f16_fp4 v123, v114, 1.0 op_sel:[1,0,0]
	v_cvt_scalef32_pk_f16_fp4 v124, v114, 1.0 op_sel:[0,1,0]
	v_cvt_scalef32_pk_f16_fp4 v125, v114, 1.0 op_sel:[1,1,0]
	v_cvt_scalef32_pk_f16_fp4 v126, v116, 1.0
	v_cvt_scalef32_pk_f16_fp4 v127, v116, 1.0 op_sel:[1,0,0]
	v_cvt_scalef32_pk_f16_fp4 v128, v116, 1.0 op_sel:[0,1,0]
	v_cvt_scalef32_pk_f16_fp4 v129, v116, 1.0 op_sel:[1,1,0]
	v_mfma_f32_16x16x32_f16 v[18:21], v[86:89], v[122:125], v[18:21]
	v_cvt_scalef32_pk_f16_fp4 v122, v117, 1.0
	v_cvt_scalef32_pk_f16_fp4 v123, v117, 1.0 op_sel:[1,0,0]
	v_cvt_scalef32_pk_f16_fp4 v124, v117, 1.0 op_sel:[0,1,0]
	v_cvt_scalef32_pk_f16_fp4 v125, v117, 1.0 op_sel:[1,1,0]
	v_mfma_f32_16x16x32_f16 v[22:25], v[86:89], v[126:129], v[22:25]
	v_cvt_scalef32_pk_f16_fp4 v126, v115, 1.0
	v_cvt_scalef32_pk_f16_fp4 v127, v115, 1.0 op_sel:[1,0,0]
	v_cvt_scalef32_pk_f16_fp4 v128, v115, 1.0 op_sel:[0,1,0]
	v_cvt_scalef32_pk_f16_fp4 v129, v115, 1.0 op_sel:[1,1,0]
	v_mfma_f32_16x16x32_f16 v[18:21], v[94:97], v[122:125], v[18:21]
	v_mfma_f32_16x16x32_f16 v[22:25], v[94:97], v[126:129], v[22:25]
	ds_read_b64_tr_b4 v[114:115], v154 offset:8192
	ds_read_b64_tr_b4 v[116:117], v162 offset:8192
	s_waitcnt lgkmcnt(2)
	v_cvt_scalef32_pk_f16_fp4 v122, v118, 1.0
	v_cvt_scalef32_pk_f16_fp4 v123, v118, 1.0 op_sel:[1,0,0]
	v_cvt_scalef32_pk_f16_fp4 v124, v118, 1.0 op_sel:[0,1,0]
	v_cvt_scalef32_pk_f16_fp4 v125, v118, 1.0 op_sel:[1,1,0]
	v_cvt_scalef32_pk_f16_fp4 v126, v120, 1.0
	v_cvt_scalef32_pk_f16_fp4 v127, v120, 1.0 op_sel:[1,0,0]
	v_cvt_scalef32_pk_f16_fp4 v128, v120, 1.0 op_sel:[0,1,0]
	v_cvt_scalef32_pk_f16_fp4 v129, v120, 1.0 op_sel:[1,1,0]
	v_mfma_f32_16x16x32_f16 v[26:29], v[86:89], v[122:125], v[26:29]
	v_cvt_scalef32_pk_f16_fp4 v122, v121, 1.0
	v_cvt_scalef32_pk_f16_fp4 v123, v121, 1.0 op_sel:[1,0,0]
	v_cvt_scalef32_pk_f16_fp4 v124, v121, 1.0 op_sel:[0,1,0]
	v_cvt_scalef32_pk_f16_fp4 v125, v121, 1.0 op_sel:[1,1,0]
	v_mfma_f32_16x16x32_f16 v[30:33], v[86:89], v[126:129], v[30:33]
	v_cvt_scalef32_pk_f16_fp4 v126, v119, 1.0
	v_cvt_scalef32_pk_f16_fp4 v127, v119, 1.0 op_sel:[1,0,0]
	v_cvt_scalef32_pk_f16_fp4 v128, v119, 1.0 op_sel:[0,1,0]
	v_cvt_scalef32_pk_f16_fp4 v129, v119, 1.0 op_sel:[1,1,0]
	v_mfma_f32_16x16x32_f16 v[26:29], v[94:97], v[122:125], v[26:29]
	v_mfma_f32_16x16x32_f16 v[30:33], v[94:97], v[126:129], v[30:33]
	ds_read_b64_tr_b4 v[118:119], v155 offset:8192
	ds_read_b64_tr_b4 v[120:121], v163 offset:8192
	s_waitcnt lgkmcnt(2)
	v_cvt_scalef32_pk_f16_fp4 v122, v114, 1.0
	v_cvt_scalef32_pk_f16_fp4 v123, v114, 1.0 op_sel:[1,0,0]
	v_cvt_scalef32_pk_f16_fp4 v124, v114, 1.0 op_sel:[0,1,0]
	v_cvt_scalef32_pk_f16_fp4 v125, v114, 1.0 op_sel:[1,1,0]
	v_cvt_scalef32_pk_f16_fp4 v126, v116, 1.0
	v_cvt_scalef32_pk_f16_fp4 v127, v116, 1.0 op_sel:[1,0,0]
	v_cvt_scalef32_pk_f16_fp4 v128, v116, 1.0 op_sel:[0,1,0]
	v_cvt_scalef32_pk_f16_fp4 v129, v116, 1.0 op_sel:[1,1,0]
	v_mfma_f32_16x16x32_f16 v[34:37], v[86:89], v[122:125], v[34:37]
	v_cvt_scalef32_pk_f16_fp4 v122, v117, 1.0
	v_cvt_scalef32_pk_f16_fp4 v123, v117, 1.0 op_sel:[1,0,0]
	v_cvt_scalef32_pk_f16_fp4 v124, v117, 1.0 op_sel:[0,1,0]
	v_cvt_scalef32_pk_f16_fp4 v125, v117, 1.0 op_sel:[1,1,0]
	v_mfma_f32_16x16x32_f16 v[38:41], v[86:89], v[126:129], v[38:41]
	v_cvt_scalef32_pk_f16_fp4 v126, v115, 1.0
	v_cvt_scalef32_pk_f16_fp4 v127, v115, 1.0 op_sel:[1,0,0]
	v_cvt_scalef32_pk_f16_fp4 v128, v115, 1.0 op_sel:[0,1,0]
	v_cvt_scalef32_pk_f16_fp4 v129, v115, 1.0 op_sel:[1,1,0]
	v_mfma_f32_16x16x32_f16 v[34:37], v[94:97], v[122:125], v[34:37]
	v_mfma_f32_16x16x32_f16 v[38:41], v[94:97], v[126:129], v[38:41]
	ds_read_b64_tr_b4 v[114:115], v156 offset:8192
	ds_read_b64_tr_b4 v[116:117], v164 offset:8192
	s_waitcnt lgkmcnt(2)
	v_cvt_scalef32_pk_f16_fp4 v122, v118, 1.0
	v_cvt_scalef32_pk_f16_fp4 v123, v118, 1.0 op_sel:[1,0,0]
	v_cvt_scalef32_pk_f16_fp4 v124, v118, 1.0 op_sel:[0,1,0]
	v_cvt_scalef32_pk_f16_fp4 v125, v118, 1.0 op_sel:[1,1,0]
	v_cvt_scalef32_pk_f16_fp4 v126, v120, 1.0
	v_cvt_scalef32_pk_f16_fp4 v127, v120, 1.0 op_sel:[1,0,0]
	v_cvt_scalef32_pk_f16_fp4 v128, v120, 1.0 op_sel:[0,1,0]
	v_cvt_scalef32_pk_f16_fp4 v129, v120, 1.0 op_sel:[1,1,0]
	v_mfma_f32_16x16x32_f16 v[42:45], v[86:89], v[122:125], v[42:45]
	v_cvt_scalef32_pk_f16_fp4 v122, v121, 1.0
	v_cvt_scalef32_pk_f16_fp4 v123, v121, 1.0 op_sel:[1,0,0]
	v_cvt_scalef32_pk_f16_fp4 v124, v121, 1.0 op_sel:[0,1,0]
	v_cvt_scalef32_pk_f16_fp4 v125, v121, 1.0 op_sel:[1,1,0]
	v_mfma_f32_16x16x32_f16 v[46:49], v[86:89], v[126:129], v[46:49]
	v_cvt_scalef32_pk_f16_fp4 v126, v119, 1.0
	v_cvt_scalef32_pk_f16_fp4 v127, v119, 1.0 op_sel:[1,0,0]
	v_cvt_scalef32_pk_f16_fp4 v128, v119, 1.0 op_sel:[0,1,0]
	v_cvt_scalef32_pk_f16_fp4 v129, v119, 1.0 op_sel:[1,1,0]
	v_mfma_f32_16x16x32_f16 v[42:45], v[94:97], v[122:125], v[42:45]
	v_mfma_f32_16x16x32_f16 v[46:49], v[94:97], v[126:129], v[46:49]
	ds_read_b64_tr_b4 v[118:119], v157 offset:8192
	ds_read_b64_tr_b4 v[120:121], v165 offset:8192
	s_waitcnt lgkmcnt(2)
	v_cvt_scalef32_pk_f16_fp4 v122, v114, 1.0
	v_cvt_scalef32_pk_f16_fp4 v123, v114, 1.0 op_sel:[1,0,0]
	v_cvt_scalef32_pk_f16_fp4 v124, v114, 1.0 op_sel:[0,1,0]
	v_cvt_scalef32_pk_f16_fp4 v125, v114, 1.0 op_sel:[1,1,0]
	v_cvt_scalef32_pk_f16_fp4 v126, v116, 1.0
	v_cvt_scalef32_pk_f16_fp4 v127, v116, 1.0 op_sel:[1,0,0]
	v_cvt_scalef32_pk_f16_fp4 v128, v116, 1.0 op_sel:[0,1,0]
	v_cvt_scalef32_pk_f16_fp4 v129, v116, 1.0 op_sel:[1,1,0]
	v_mfma_f32_16x16x32_f16 v[50:53], v[86:89], v[122:125], v[50:53]
	v_cvt_scalef32_pk_f16_fp4 v122, v117, 1.0
	v_cvt_scalef32_pk_f16_fp4 v123, v117, 1.0 op_sel:[1,0,0]
	v_cvt_scalef32_pk_f16_fp4 v124, v117, 1.0 op_sel:[0,1,0]
	v_cvt_scalef32_pk_f16_fp4 v125, v117, 1.0 op_sel:[1,1,0]
	v_mfma_f32_16x16x32_f16 v[54:57], v[86:89], v[126:129], v[54:57]
	v_cvt_scalef32_pk_f16_fp4 v126, v115, 1.0
	v_cvt_scalef32_pk_f16_fp4 v127, v115, 1.0 op_sel:[1,0,0]
	v_cvt_scalef32_pk_f16_fp4 v128, v115, 1.0 op_sel:[0,1,0]
	v_cvt_scalef32_pk_f16_fp4 v129, v115, 1.0 op_sel:[1,1,0]
	v_mfma_f32_16x16x32_f16 v[50:53], v[94:97], v[122:125], v[50:53]
	v_mfma_f32_16x16x32_f16 v[54:57], v[94:97], v[126:129], v[54:57]
	s_waitcnt vmcnt(0)
	ds_read_b64_tr_b4 v[114:115], v150
	ds_read_b64_tr_b4 v[116:117], v158
	s_waitcnt lgkmcnt(2)
	s_add_i32 m0, s38, 0x2000
	v_mad_u32_u16 v178, v102, v198, v166
	global_load_lds_dwordx4 v178, s[40:41]
	s_add_i32 m0, s38, 0x2400
	v_mad_u32_u16 v179, v102, v198, v167 op_sel:[1,0,0,0]
	global_load_lds_dwordx4 v179, s[40:41]
	s_add_i32 m0, s38, 0x2800
	v_mad_u32_u16 v178, v103, v198, v168
	global_load_lds_dwordx4 v178, s[40:41]
	s_add_i32 m0, s38, 0x2c00
	v_mad_u32_u16 v179, v103, v198, v169 op_sel:[1,0,0,0]
	global_load_lds_dwordx4 v179, s[40:41]
	s_add_i32 m0, s38, 0x3000
	v_mad_u32_u16 v178, v104, v198, v170
	global_load_lds_dwordx4 v178, s[40:41]
	s_add_i32 m0, s38, 0x3400
	v_mad_u32_u16 v179, v104, v198, v171 op_sel:[1,0,0,0]
	global_load_lds_dwordx4 v179, s[40:41]
	s_add_i32 m0, s38, 0x3800
	v_mad_u32_u16 v178, v105, v198, v172
	global_load_lds_dwordx4 v178, s[40:41]
	s_add_i32 m0, s38, 0x3c00
	v_mad_u32_u16 v179, v105, v198, v173 op_sel:[1,0,0,0]
	global_load_lds_dwordx4 v179, s[40:41]
	ds_read_b128 v[66:69], v174
	ds_read_b128 v[70:73], v174 offset:16
	ds_read_b128 v[74:77], v175
	ds_read_b128 v[78:81], v175 offset:16
	ds_read_b128 v[106:109], v199 offset:256
	ds_read_b128 v[110:113], v199 offset:272
	v_cvt_scalef32_pk_f16_fp4 v122, v118, 1.0
	v_cvt_scalef32_pk_f16_fp4 v123, v118, 1.0 op_sel:[1,0,0]
	v_cvt_scalef32_pk_f16_fp4 v124, v118, 1.0 op_sel:[0,1,0]
	v_cvt_scalef32_pk_f16_fp4 v125, v118, 1.0 op_sel:[1,1,0]
	v_cvt_scalef32_pk_f16_fp4 v126, v120, 1.0
	v_cvt_scalef32_pk_f16_fp4 v127, v120, 1.0 op_sel:[1,0,0]
	v_cvt_scalef32_pk_f16_fp4 v128, v120, 1.0 op_sel:[0,1,0]
	v_cvt_scalef32_pk_f16_fp4 v129, v120, 1.0 op_sel:[1,1,0]
	v_mfma_f32_16x16x32_f16 v[58:61], v[86:89], v[122:125], v[58:61]
	v_cvt_scalef32_pk_f16_fp4 v122, v121, 1.0
	v_cvt_scalef32_pk_f16_fp4 v123, v121, 1.0 op_sel:[1,0,0]
	v_cvt_scalef32_pk_f16_fp4 v124, v121, 1.0 op_sel:[0,1,0]
	v_cvt_scalef32_pk_f16_fp4 v125, v121, 1.0 op_sel:[1,1,0]
	v_mfma_f32_16x16x32_f16 v[62:65], v[86:89], v[126:129], v[62:65]
	v_cvt_scalef32_pk_f16_fp4 v126, v119, 1.0
	v_cvt_scalef32_pk_f16_fp4 v127, v119, 1.0 op_sel:[1,0,0]
	v_cvt_scalef32_pk_f16_fp4 v128, v119, 1.0 op_sel:[0,1,0]
	v_cvt_scalef32_pk_f16_fp4 v129, v119, 1.0 op_sel:[1,1,0]
	v_mfma_f32_16x16x32_f16 v[58:61], v[94:97], v[122:125], v[58:61]
	v_mfma_f32_16x16x32_f16 v[62:65], v[94:97], v[126:129], v[62:65]
	s_nop 7
	v_cmp_ne_u32_e32 vcc, 0, v196
	v_cndmask_b32_e32 v146, v2, v6, vcc
	v_cndmask_b32_e32 v142, v10, v14, vcc
	v_cndmask_b32_e32 v147, v18, v22, vcc
	v_cndmask_b32_e32 v143, v26, v30, vcc
	v_cndmask_b32_e32 v148, v34, v38, vcc
	v_cndmask_b32_e32 v144, v42, v46, vcc
	v_cndmask_b32_e32 v149, v50, v54, vcc
	v_cndmask_b32_e32 v145, v58, v62, vcc
	v_cmp_ne_u32_e32 vcc, 0, v197
	v_cndmask_b32_e32 v146, v146, v142, vcc
	v_cndmask_b32_e32 v147, v147, v143, vcc
	v_cndmask_b32_e32 v148, v148, v144, vcc
	v_cndmask_b32_e32 v149, v149, v145, vcc
	v_fma_f32 v142, v134, v146, v130
	v_fma_f32 v143, v135, v147, v131
	v_fma_f32 v144, v136, v148, v132
	v_fma_f32 v145, v137, v149, v133
	global_store_dword v[180:181], v142, off
	global_store_dword v[180:181], v143, off offset:256
	global_store_dword v[180:181], v144, off offset:512
	global_store_dword v[180:181], v145, off offset:768
	v_lshl_add_u64 v[180:181], v[180:181], 0, s[48:49]
	s_add_i32 s33, s33, 2
	s_cmp_lt_u32 s33, 8
	s_cbranch_scc1 .Le2_loop
	s_cmp_lt_i32 s35, 0
	s_cbranch_scc1 .Le2_exit
	s_add_i32 s39, s39, s43
	s_add_i32 s39, s39, 7
	v_mov_b32_e32 v180, v182
	v_mov_b32_e32 v181, v183
	v_mov_b32_e32 v134, v138
	v_mov_b32_e32 v135, v139
	v_mov_b32_e32 v136, v140
	v_mov_b32_e32 v137, v141
	s_mov_b32 s33, 0
	s_branch .Le2_loop
